# v7 plus: FoxIn epilogue row-scale reduction batched + its partial-sum loads hoisted before the K-loop; residual epilogues (ph8, ph12) use global ops with counted vmcnt instead of full drains; attentio
# speedup vs baseline: 1.0207x; 1.0031x over previous
.LBB0_927:
	s_lshl_b32 s58, s29, 8
	v_add_u32_e32 v28, s58, v199
	s_nop 15
	s_nop 7
	v_lshl_or_b32 v26, s28, 8, v201
	v_ashrrev_i32_e32 v29, 31, v28
	v_ashrrev_i32_e32 v27, 31, v26
	v_lshlrev_b64 v[18:19], 11, v[28:29]
	v_lshl_add_u64 v[18:19], s[26:27], 0, v[18:19]
	v_lshlrev_b64 v[30:31], 1, v[26:27]
	s_waitcnt lgkmcnt(0)
	v_lshl_add_u64 v[2:3], v[26:27], 2, s[36:37]
	v_lshl_add_u64 v[186:187], v[18:19], 0, v[30:31]
	global_load_dwordx4 v[14:17] v[2:3], off
	global_load_dwordx4 v[10:13] v[2:3], off offset:16
	global_load_dwordx4 v[6:9] v[2:3], off offset:512
	s_nop 0
	global_load_dwordx4 v[2:5] v[2:3], off offset:528
	s_nop 0
	global_load_dwordx4 v[18:21] v[186:187], off
	global_load_dwordx4 v[22:25] v[186:187], off offset:256
	v_lshlrev_b64 v[32:33], 10, v[28:29]
	v_lshl_add_u64 v[196:197], v[32:33], 0, v[26:27]
	v_add_u32_e32 v32, 16, v28
	v_ashrrev_i32_e32 v33, 31, v32
	s_waitcnt vmcnt(0) lgkmcnt(0)
	v_lshlrev_b32_e32 v170, 16, v18
	v_and_b32_e32 v171, 0xffff0000, v18
	v_lshlrev_b32_e32 v172, 16, v19
	v_and_b32_e32 v173, 0xffff0000, v19
	v_lshlrev_b64 v[18:19], 11, v[32:33]
	v_lshl_add_u64 v[18:19], s[26:27], 0, v[18:19]
	v_lshl_add_u64 v[30:31], v[18:19], 0, v[30:31]
	v_lshlrev_b32_e32 v174, 16, v20
	v_and_b32_e32 v175, 0xffff0000, v20
	v_lshlrev_b32_e32 v176, 16, v21
	v_and_b32_e32 v177, 0xffff0000, v21
	v_lshlrev_b32_e32 v192, 16, v22
	v_and_b32_e32 v193, 0xffff0000, v22
	v_lshlrev_b32_e32 v194, 16, v23
	v_and_b32_e32 v195, 0xffff0000, v23
	v_lshlrev_b32_e32 v188, 16, v24
	v_and_b32_e32 v189, 0xffff0000, v24
	v_lshlrev_b32_e32 v190, 16, v25
	v_and_b32_e32 v191, 0xffff0000, v25
	global_load_dwordx4 v[22:25] v[30:31], off
	global_load_dwordx4 v[18:21] v[30:31], off offset:256
	v_pk_add_f32 v[160:161], v[160:161], v[172:173]
	v_pk_add_f32 v[158:159], v[158:159], v[170:171]
	v_pk_add_f32 v[172:173], v[154:155], v[174:175]
	v_cvt_pk_bf16_f32 v154, v158, v159
	v_pk_add_f32 v[170:171], v[156:157], v[176:177]
	v_cvt_pk_bf16_f32 v155, v160, v161
	v_cvt_pk_bf16_f32 v156, v172, v173
	v_mul_f32_e32 v29, v159, v159
	v_cvt_pk_bf16_f32 v157, v170, v171
	global_store_dwordx4 v[186:187], v[154:157], off
	v_fmac_f32_e32 v29, v158, v158
	v_pk_mul_f32 v[158:159], v[14:15], v[158:159]
	v_mul_f32_e32 v154, v161, v161
	v_fmac_f32_e32 v154, v160, v160
	v_add_f32_e32 v29, v29, v154
	v_mul_f32_e32 v154, v173, v173
	v_fmac_f32_e32 v154, v172, v172
	v_add_f32_e32 v29, v154, v29
	v_mul_f32_e32 v154, v171, v171
	v_fmac_f32_e32 v154, v170, v170
	v_mul_f32_e32 v158, 4.0, v158
	v_add_f32_e32 v29, v154, v29
	v_pk_mul_f32 v[160:161], v[16:17], v[160:161]
	v_pk_mul_f32 v[154:155], v[12:13], v[170:171]
	v_med3_f32 v170, v158, s87, v227
	v_mul_f32_e32 v158, 4.0, v159
	v_med3_f32 v159, v158, s87, v227
	v_mul_f32_e32 v158, 4.0, v160
	v_pk_mul_f32 v[156:157], v[10:11], v[172:173]
	v_med3_f32 v160, v158, s87, v227
	v_mul_f32_e32 v158, 4.0, v161
	v_med3_f32 v161, v158, s87, v227
	v_mov_b32_e32 v158, v167
	v_mul_f32_e32 v156, 4.0, v156
	v_mul_f32_e32 v157, 4.0, v157
	v_cvt_pk_fp8_f32 v158, v170, v159
	v_med3_f32 v156, v156, s87, v227
	v_med3_f32 v157, v157, s87, v227
	v_mov_b32_e32 v159, v167
	v_cvt_pk_fp8_f32 v159, v156, v157
	v_mul_f32_e32 v154, 4.0, v154
	v_mul_f32_e32 v155, 4.0, v155
	v_med3_f32 v154, v154, s87, v227
	v_med3_f32 v155, v155, s87, v227
	v_cvt_pk_fp8_f32 v158, v160, v161 op_sel:[0,0,1]
	v_cvt_pk_fp8_f32 v159, v154, v155 op_sel:[0,0,1]
	v_lshl_add_u64 v[154:155], s[34:35], 0, v[196:197]
	v_pk_add_f32 v[152:153], v[152:153], v[194:195]
	v_pk_add_f32 v[150:151], v[150:151], v[192:193]
	global_store_dwordx2 v[154:155], v[158:159], off
	v_pk_add_f32 v[158:159], v[146:147], v[188:189]
	v_cvt_pk_bf16_f32 v146, v150, v151
	v_cvt_pk_bf16_f32 v147, v152, v153
	v_pk_add_f32 v[156:157], v[148:149], v[190:191]
	v_cvt_pk_bf16_f32 v148, v158, v159
	s_nop 0
	v_cvt_pk_bf16_f32 v149, v156, v157
	global_store_dwordx4 v[186:187], v[146:149], off offset:256
	s_nop 1
	v_mul_f32_e32 v146, v151, v151
	v_mul_f32_e32 v147, v153, v153
	v_fmac_f32_e32 v146, v150, v150
	v_fmac_f32_e32 v147, v152, v152
	v_add_f32_e32 v146, v146, v147
	v_mul_f32_e32 v147, v159, v159
	v_fmac_f32_e32 v147, v158, v158
	v_add_f32_e32 v146, v147, v146
	v_mul_f32_e32 v147, v157, v157
	v_fmac_f32_e32 v147, v156, v156
	v_add_f32_e32 v146, v147, v146
	v_add_f32_e32 v29, v29, v146
	v_pk_mul_f32 v[146:147], v[8:9], v[152:153]
	v_pk_mul_f32 v[148:149], v[6:7], v[150:151]
	v_mul_f32_e32 v146, 4.0, v146
	v_pk_mul_f32 v[150:151], v[4:5], v[156:157]
	v_mul_f32_e32 v148, 4.0, v148
	v_mul_f32_e32 v149, 4.0, v149
	v_med3_f32 v156, v146, s87, v227
	v_mul_f32_e32 v146, 4.0, v147
	v_med3_f32 v148, v148, s87, v227
	v_med3_f32 v149, v149, s87, v227
	v_med3_f32 v147, v146, s87, v227
	v_mov_b32_e32 v146, v167
	v_cvt_pk_fp8_f32 v146, v148, v149
	v_pk_mul_f32 v[152:153], v[2:3], v[158:159]
	v_cvt_pk_fp8_f32 v146, v156, v147 op_sel:[0,0,1]
	v_mul_f32_e32 v147, 4.0, v152
	v_med3_f32 v148, v147, s87, v227
	v_mul_f32_e32 v147, 4.0, v153
	v_med3_f32 v149, v147, s87, v227
	v_mul_f32_e32 v147, 4.0, v150
	v_med3_f32 v150, v147, s87, v227
	v_mul_f32_e32 v147, 4.0, v151
	v_med3_f32 v151, v147, s87, v227
	v_mov_b32_e32 v147, v167
	v_cvt_pk_fp8_f32 v147, v148, v149
	v_cvt_pk_fp8_f32 v147, v150, v151 op_sel:[0,0,1]
	global_store_dwordx2 v[154:155], v[146:147], off offset:128
	v_and_b32_e32 v147, 64, v231
	v_xor_b32_e32 v146, 16, v231
	v_add_u32_e32 v147, 64, v147
	v_cmp_lt_i32_e32 vcc, v146, v147
	s_nop 1
	v_cndmask_b32_e32 v146, v231, v146, vcc
	v_lshlrev_b32_e32 v148, 2, v146
	ds_bpermute_b32 v146, v148, v29
	s_waitcnt lgkmcnt(0)
	v_add_f32_e32 v29, v29, v146
	v_xor_b32_e32 v146, 32, v231
	v_cmp_lt_i32_e32 vcc, v146, v147
	s_nop 1
	v_cndmask_b32_e32 v146, v231, v146, vcc
	v_lshlrev_b32_e32 v149, 2, v146
	ds_bpermute_b32 v146, v149, v29
	s_and_saveexec_b64 s[60:61], s[38:39]
	s_cbranch_execz .LBB0_929
	s_waitcnt lgkmcnt(0)
	v_add_f32_e32 v29, v29, v146
	ds_write_b32 v202, v29
.LBB0_929:
	s_or_b64 exec, exec, s[60:61]
	s_waitcnt lgkmcnt(0)
	v_add_u32_e32 v146, 32, v28
	v_ashrrev_i32_e32 v147, 31, v146
	s_waitcnt vmcnt(4)
	v_lshlrev_b32_e32 v158, 16, v18
	v_and_b32_e32 v159, 0xffff0000, v18
	v_lshlrev_b32_e32 v160, 16, v19
	v_and_b32_e32 v161, 0xffff0000, v19
	v_lshlrev_b64 v[18:19], 11, v[146:147]
	v_lshlrev_b64 v[32:33], 10, v[32:33]
	v_lshl_add_u64 v[18:19], s[26:27], 0, v[18:19]
	v_lshl_add_u64 v[174:175], v[32:33], 0, v[26:27]
	v_lshl_add_u64 v[32:33], v[26:27], 1, v[18:19]
	v_lshlrev_b32_e32 v150, 16, v22
	v_and_b32_e32 v151, 0xffff0000, v22
	v_lshlrev_b32_e32 v152, 16, v23
	v_and_b32_e32 v153, 0xffff0000, v23
	v_lshlrev_b32_e32 v154, 16, v24
	v_and_b32_e32 v155, 0xffff0000, v24
	v_lshlrev_b32_e32 v156, 16, v25
	v_and_b32_e32 v157, 0xffff0000, v25
	v_lshlrev_b32_e32 v170, 16, v20
	v_and_b32_e32 v171, 0xffff0000, v20
	v_lshlrev_b32_e32 v172, 16, v21
	v_and_b32_e32 v173, 0xffff0000, v21
	global_load_dwordx4 v[22:25] v[32:33], off
	global_load_dwordx4 v[18:21] v[32:33], off offset:256
	v_pk_add_f32 v[144:145], v[144:145], v[152:153]
	v_pk_add_f32 v[142:143], v[142:143], v[150:151]
	v_pk_add_f32 v[152:153], v[138:139], v[154:155]
	v_cvt_pk_bf16_f32 v138, v142, v143
	v_pk_add_f32 v[150:151], v[140:141], v[156:157]
	v_cvt_pk_bf16_f32 v139, v144, v145
	v_cvt_pk_bf16_f32 v140, v152, v153
	v_mul_f32_e32 v29, v143, v143
	v_cvt_pk_bf16_f32 v141, v150, v151
	global_store_dwordx4 v[30:31], v[138:141], off
	v_fmac_f32_e32 v29, v142, v142
	v_mul_f32_e32 v154, v151, v151
	v_mul_f32_e32 v138, v145, v145
	v_fmac_f32_e32 v138, v144, v144
	v_add_f32_e32 v29, v29, v138
	v_mul_f32_e32 v138, v153, v153
	v_fmac_f32_e32 v138, v152, v152
	v_pk_mul_f32 v[140:141], v[14:15], v[142:143]
	v_add_f32_e32 v29, v138, v29
	v_pk_mul_f32 v[138:139], v[16:17], v[144:145]
	v_mul_f32_e32 v140, 4.0, v140
	v_mul_f32_e32 v141, 4.0, v141
	v_pk_mul_f32 v[142:143], v[12:13], v[150:151]
	v_med3_f32 v140, v140, s87, v227
	v_med3_f32 v141, v141, s87, v227
	v_mul_f32_e32 v151, 4.0, v138
	v_mov_b32_e32 v138, v167
	v_cvt_pk_fp8_f32 v138, v140, v141
	v_mul_f32_e32 v139, 4.0, v139
	v_pk_mul_f32 v[144:145], v[10:11], v[152:153]
	v_med3_f32 v140, v151, s87, v227
	v_med3_f32 v139, v139, s87, v227
	v_cvt_pk_fp8_f32 v138, v140, v139 op_sel:[0,0,1]
	v_mul_f32_e32 v139, 4.0, v144
	v_med3_f32 v140, v139, s87, v227
	v_mul_f32_e32 v139, 4.0, v145
	v_med3_f32 v141, v139, s87, v227
	v_mov_b32_e32 v139, v167
	v_cvt_pk_fp8_f32 v139, v140, v141
	v_mul_f32_e32 v142, 4.0, v142
	v_mul_f32_e32 v141, 4.0, v143
	v_med3_f32 v140, v142, s87, v227
	v_med3_f32 v141, v141, s87, v227
	v_cvt_pk_fp8_f32 v139, v140, v141 op_sel:[0,0,1]
	v_pk_add_f32 v[136:137], v[136:137], v[160:161]
	v_pk_add_f32 v[134:135], v[134:135], v[158:159]
	v_pk_add_f32 v[142:143], v[130:131], v[170:171]
	v_mul_f32_e32 v130, v135, v135
	v_mul_f32_e32 v131, v137, v137
	v_fmac_f32_e32 v130, v134, v134
	v_fmac_f32_e32 v131, v136, v136
	v_lshl_add_u64 v[140:141], s[34:35], 0, v[174:175]
	v_add_f32_e32 v130, v130, v131
	v_mul_f32_e32 v131, v143, v143
	global_store_dwordx2 v[140:141], v[138:139], off
	v_pk_add_f32 v[138:139], v[132:133], v[172:173]
	v_cvt_pk_bf16_f32 v132, v134, v135
	v_fmac_f32_e32 v131, v142, v142
	v_pk_mul_f32 v[134:135], v[6:7], v[134:135]
	v_add_f32_e32 v130, v131, v130
	v_mul_f32_e32 v131, v139, v139
	v_mul_f32_e32 v134, 4.0, v134
	v_mul_f32_e32 v135, 4.0, v135
	v_fmac_f32_e32 v154, v150, v150
	v_fmac_f32_e32 v131, v138, v138
	v_med3_f32 v134, v134, s87, v227
	v_med3_f32 v135, v135, s87, v227
	v_mov_b32_e32 v150, v167
	v_add_f32_e32 v29, v154, v29
	v_add_f32_e32 v130, v131, v130
	v_cvt_pk_fp8_f32 v150, v134, v135
	v_add_f32_e32 v29, v29, v130
	v_pk_mul_f32 v[130:131], v[8:9], v[136:137]
	v_pk_mul_f32 v[144:145], v[2:3], v[142:143]
	v_mul_f32_e32 v130, 4.0, v130
	v_mul_f32_e32 v131, 4.0, v131
	v_med3_f32 v130, v130, s87, v227
	v_med3_f32 v131, v131, s87, v227
	v_cvt_pk_fp8_f32 v150, v130, v131 op_sel:[0,0,1]
	v_mul_f32_e32 v130, 4.0, v144
	v_mul_f32_e32 v131, 4.0, v145
	v_med3_f32 v130, v130, s87, v227
	v_med3_f32 v131, v131, s87, v227
	v_mov_b32_e32 v151, v167
	v_cvt_pk_fp8_f32 v151, v130, v131
	ds_bpermute_b32 v130, v148, v29
	v_cvt_pk_bf16_f32 v133, v136, v137
	v_pk_mul_f32 v[136:137], v[4:5], v[138:139]
	s_waitcnt lgkmcnt(0)
	v_add_f32_e32 v29, v29, v130
	v_mul_f32_e32 v134, 4.0, v136
	v_med3_f32 v131, v134, s87, v227
	v_mul_f32_e32 v134, 4.0, v137
	ds_bpermute_b32 v130, v149, v29
	v_med3_f32 v134, v134, s87, v227
	v_cvt_pk_fp8_f32 v151, v131, v134 op_sel:[0,0,1]
	v_cvt_pk_bf16_f32 v134, v142, v143
	v_cvt_pk_bf16_f32 v135, v138, v139
	global_store_dwordx4 v[30:31], v[132:135], off offset:256
	global_store_dwordx2 v[140:141], v[150:151], off offset:128
	s_and_saveexec_b64 s[60:61], s[38:39]
	s_cbranch_execz .LBB0_931
	s_waitcnt lgkmcnt(0)
	v_add_f32_e32 v29, v29, v130
	ds_write_b32 v202, v29 offset:64
.LBB0_931:
	s_or_b64 exec, exec, s[60:61]
	s_waitcnt lgkmcnt(0)
	v_add_u32_e32 v130, 48, v28
	v_ashrrev_i32_e32 v131, 31, v130
	s_waitcnt vmcnt(4)
	v_lshlrev_b32_e32 v140, 16, v18
	v_and_b32_e32 v141, 0xffff0000, v18
	v_lshlrev_b32_e32 v142, 16, v19
	v_and_b32_e32 v143, 0xffff0000, v19
	v_lshlrev_b64 v[18:19], 11, v[130:131]
	v_lshlrev_b64 v[30:31], 10, v[146:147]
	v_lshl_add_u64 v[18:19], s[26:27], 0, v[18:19]
	v_lshl_add_u64 v[150:151], v[30:31], 0, v[26:27]
	v_lshl_add_u64 v[30:31], v[26:27], 1, v[18:19]
	v_lshlrev_b32_e32 v132, 16, v22
	v_and_b32_e32 v133, 0xffff0000, v22
	v_lshlrev_b32_e32 v134, 16, v23
	v_and_b32_e32 v135, 0xffff0000, v23
	v_lshlrev_b32_e32 v136, 16, v24
	v_and_b32_e32 v137, 0xffff0000, v24
	v_lshlrev_b32_e32 v138, 16, v25
	v_and_b32_e32 v139, 0xffff0000, v25
	v_lshlrev_b32_e32 v144, 16, v20
	v_and_b32_e32 v145, 0xffff0000, v20
	v_lshlrev_b32_e32 v146, 16, v21
	v_and_b32_e32 v147, 0xffff0000, v21
	global_load_dwordx4 v[22:25] v[30:31], off
	global_load_dwordx4 v[18:21] v[30:31], off offset:256
	v_pk_add_f32 v[128:129], v[128:129], v[134:135]
	v_pk_add_f32 v[126:127], v[126:127], v[132:133]
	v_pk_add_f32 v[134:135], v[122:123], v[136:137]
	v_cvt_pk_bf16_f32 v122, v126, v127
	v_pk_add_f32 v[132:133], v[124:125], v[138:139]
	v_cvt_pk_bf16_f32 v123, v128, v129
	v_cvt_pk_bf16_f32 v124, v134, v135
	v_mul_f32_e32 v29, v127, v127
	v_cvt_pk_bf16_f32 v125, v132, v133
	global_store_dwordx4 v[32:33], v[122:125], off
	v_fmac_f32_e32 v29, v126, v126
	v_mul_f32_e32 v136, v133, v133
	v_mul_f32_e32 v122, v129, v129
	v_fmac_f32_e32 v122, v128, v128
	v_add_f32_e32 v29, v29, v122
	v_mul_f32_e32 v122, v135, v135
	v_fmac_f32_e32 v122, v134, v134
	v_pk_mul_f32 v[124:125], v[14:15], v[126:127]
	v_add_f32_e32 v29, v122, v29
	v_pk_mul_f32 v[122:123], v[16:17], v[128:129]
	v_mul_f32_e32 v124, 4.0, v124
	v_mul_f32_e32 v125, 4.0, v125
	v_pk_mul_f32 v[126:127], v[12:13], v[132:133]
	v_med3_f32 v124, v124, s87, v227
	v_med3_f32 v125, v125, s87, v227
	v_mul_f32_e32 v133, 4.0, v122
	v_mov_b32_e32 v122, v167
	v_cvt_pk_fp8_f32 v122, v124, v125
	v_mul_f32_e32 v123, 4.0, v123
	v_pk_mul_f32 v[128:129], v[10:11], v[134:135]
	v_med3_f32 v124, v133, s87, v227
	v_med3_f32 v123, v123, s87, v227
	v_cvt_pk_fp8_f32 v122, v124, v123 op_sel:[0,0,1]
	v_mul_f32_e32 v123, 4.0, v128
	v_med3_f32 v124, v123, s87, v227
	v_mul_f32_e32 v123, 4.0, v129
	v_med3_f32 v125, v123, s87, v227
	v_mov_b32_e32 v123, v167
	v_cvt_pk_fp8_f32 v123, v124, v125
	v_mul_f32_e32 v126, 4.0, v126
	v_mul_f32_e32 v125, 4.0, v127
	v_med3_f32 v124, v126, s87, v227
	v_med3_f32 v125, v125, s87, v227
	v_cvt_pk_fp8_f32 v123, v124, v125 op_sel:[0,0,1]
	v_pk_add_f32 v[120:121], v[120:121], v[142:143]
	v_pk_add_f32 v[118:119], v[118:119], v[140:141]
	v_pk_add_f32 v[126:127], v[114:115], v[144:145]
	v_mul_f32_e32 v114, v119, v119
	v_mul_f32_e32 v115, v121, v121
	v_fmac_f32_e32 v114, v118, v118
	v_fmac_f32_e32 v115, v120, v120
	v_lshl_add_u64 v[124:125], s[34:35], 0, v[150:151]
	v_add_f32_e32 v114, v114, v115
	v_mul_f32_e32 v115, v127, v127
	global_store_dwordx2 v[124:125], v[122:123], off
	v_pk_add_f32 v[122:123], v[116:117], v[146:147]
	v_cvt_pk_bf16_f32 v116, v118, v119
	v_fmac_f32_e32 v115, v126, v126
	v_pk_mul_f32 v[118:119], v[6:7], v[118:119]
	v_add_f32_e32 v114, v115, v114
	v_mul_f32_e32 v115, v123, v123
	v_mul_f32_e32 v118, 4.0, v118
	v_mul_f32_e32 v119, 4.0, v119
	v_fmac_f32_e32 v136, v132, v132
	v_fmac_f32_e32 v115, v122, v122
	v_med3_f32 v118, v118, s87, v227
	v_med3_f32 v119, v119, s87, v227
	v_mov_b32_e32 v132, v167
	v_add_f32_e32 v29, v136, v29
	v_add_f32_e32 v114, v115, v114
	v_cvt_pk_fp8_f32 v132, v118, v119
	v_add_f32_e32 v29, v29, v114
	v_pk_mul_f32 v[114:115], v[8:9], v[120:121]
	v_pk_mul_f32 v[128:129], v[2:3], v[126:127]
	v_mul_f32_e32 v114, 4.0, v114
	v_mul_f32_e32 v115, 4.0, v115
	v_med3_f32 v114, v114, s87, v227
	v_med3_f32 v115, v115, s87, v227
	v_cvt_pk_fp8_f32 v132, v114, v115 op_sel:[0,0,1]
	v_mul_f32_e32 v114, 4.0, v128
	v_mul_f32_e32 v115, 4.0, v129
	v_med3_f32 v114, v114, s87, v227
	v_med3_f32 v115, v115, s87, v227
	v_mov_b32_e32 v133, v167
	v_cvt_pk_fp8_f32 v133, v114, v115
	ds_bpermute_b32 v114, v148, v29
	v_cvt_pk_bf16_f32 v117, v120, v121
	v_pk_mul_f32 v[120:121], v[4:5], v[122:123]
	s_waitcnt lgkmcnt(0)
	v_add_f32_e32 v29, v29, v114
	v_mul_f32_e32 v118, 4.0, v120
	v_med3_f32 v115, v118, s87, v227
	v_mul_f32_e32 v118, 4.0, v121
	ds_bpermute_b32 v114, v149, v29
	v_med3_f32 v118, v118, s87, v227
	v_cvt_pk_fp8_f32 v133, v115, v118 op_sel:[0,0,1]
	v_cvt_pk_bf16_f32 v118, v126, v127
	v_cvt_pk_bf16_f32 v119, v122, v123
	global_store_dwordx4 v[32:33], v[116:119], off offset:256
	global_store_dwordx2 v[124:125], v[132:133], off offset:128
	s_and_saveexec_b64 s[60:61], s[38:39]
	s_cbranch_execz .LBB0_933
	s_waitcnt lgkmcnt(0)
	v_add_f32_e32 v29, v29, v114
	ds_write_b32 v202, v29 offset:128
.LBB0_933:
	s_or_b64 exec, exec, s[60:61]
	s_waitcnt lgkmcnt(0)
	v_add_u32_e32 v114, 0x80, v28
	v_ashrrev_i32_e32 v115, 31, v114
	s_waitcnt vmcnt(4)
	v_lshlrev_b32_e32 v124, 16, v18
	v_and_b32_e32 v125, 0xffff0000, v18
	v_lshlrev_b32_e32 v126, 16, v19
	v_and_b32_e32 v127, 0xffff0000, v19
	v_lshlrev_b64 v[18:19], 11, v[114:115]
	v_lshlrev_b64 v[32:33], 10, v[130:131]
	v_lshl_add_u64 v[18:19], s[26:27], 0, v[18:19]
	v_lshl_add_u64 v[132:133], v[32:33], 0, v[26:27]
	v_lshl_add_u64 v[32:33], v[26:27], 1, v[18:19]
	v_lshlrev_b32_e32 v116, 16, v22
	v_and_b32_e32 v117, 0xffff0000, v22
	v_lshlrev_b32_e32 v118, 16, v23
	v_and_b32_e32 v119, 0xffff0000, v23
	v_lshlrev_b32_e32 v120, 16, v24
	v_and_b32_e32 v121, 0xffff0000, v24
	v_lshlrev_b32_e32 v122, 16, v25
	v_and_b32_e32 v123, 0xffff0000, v25
	v_lshlrev_b32_e32 v128, 16, v20
	v_and_b32_e32 v129, 0xffff0000, v20
	v_lshlrev_b32_e32 v130, 16, v21
	v_and_b32_e32 v131, 0xffff0000, v21
	global_load_dwordx4 v[22:25] v[32:33], off
	global_load_dwordx4 v[18:21] v[32:33], off offset:256
	v_pk_add_f32 v[112:113], v[112:113], v[118:119]
	v_pk_add_f32 v[110:111], v[110:111], v[116:117]
	v_pk_add_f32 v[118:119], v[106:107], v[120:121]
	v_cvt_pk_bf16_f32 v106, v110, v111
	v_pk_add_f32 v[116:117], v[108:109], v[122:123]
	v_cvt_pk_bf16_f32 v107, v112, v113
	v_cvt_pk_bf16_f32 v108, v118, v119
	v_mul_f32_e32 v29, v111, v111
	v_cvt_pk_bf16_f32 v109, v116, v117
	global_store_dwordx4 v[30:31], v[106:109], off
	v_fmac_f32_e32 v29, v110, v110
	v_mul_f32_e32 v120, v117, v117
	v_mul_f32_e32 v106, v113, v113
	v_fmac_f32_e32 v106, v112, v112
	v_add_f32_e32 v29, v29, v106
	v_mul_f32_e32 v106, v119, v119
	v_fmac_f32_e32 v106, v118, v118
	v_pk_mul_f32 v[108:109], v[14:15], v[110:111]
	v_add_f32_e32 v29, v106, v29
	v_pk_mul_f32 v[106:107], v[16:17], v[112:113]
	v_mul_f32_e32 v108, 4.0, v108
	v_mul_f32_e32 v109, 4.0, v109
	v_pk_mul_f32 v[110:111], v[12:13], v[116:117]
	v_med3_f32 v108, v108, s87, v227
	v_med3_f32 v109, v109, s87, v227
	v_mul_f32_e32 v117, 4.0, v106
	v_mov_b32_e32 v106, v167
	v_cvt_pk_fp8_f32 v106, v108, v109
	v_mul_f32_e32 v107, 4.0, v107
	v_pk_mul_f32 v[112:113], v[10:11], v[118:119]
	v_med3_f32 v108, v117, s87, v227
	v_med3_f32 v107, v107, s87, v227
	v_cvt_pk_fp8_f32 v106, v108, v107 op_sel:[0,0,1]
	v_mul_f32_e32 v107, 4.0, v112
	v_med3_f32 v108, v107, s87, v227
	v_mul_f32_e32 v107, 4.0, v113
	v_med3_f32 v109, v107, s87, v227
	v_mov_b32_e32 v107, v167
	v_cvt_pk_fp8_f32 v107, v108, v109
	v_mul_f32_e32 v110, 4.0, v110
	v_mul_f32_e32 v109, 4.0, v111
	v_med3_f32 v108, v110, s87, v227
	v_med3_f32 v109, v109, s87, v227
	v_cvt_pk_fp8_f32 v107, v108, v109 op_sel:[0,0,1]
	v_pk_add_f32 v[104:105], v[104:105], v[126:127]
	v_pk_add_f32 v[102:103], v[102:103], v[124:125]
	v_pk_add_f32 v[110:111], v[98:99], v[128:129]
	v_mul_f32_e32 v98, v103, v103
	v_mul_f32_e32 v99, v105, v105
	v_fmac_f32_e32 v98, v102, v102
	v_fmac_f32_e32 v99, v104, v104
	v_lshl_add_u64 v[108:109], s[34:35], 0, v[132:133]
	v_add_f32_e32 v98, v98, v99
	v_mul_f32_e32 v99, v111, v111
	global_store_dwordx2 v[108:109], v[106:107], off
	v_pk_add_f32 v[106:107], v[100:101], v[130:131]
	v_cvt_pk_bf16_f32 v100, v102, v103
	v_fmac_f32_e32 v99, v110, v110
	v_pk_mul_f32 v[102:103], v[6:7], v[102:103]
	v_add_f32_e32 v98, v99, v98
	v_mul_f32_e32 v99, v107, v107
	v_mul_f32_e32 v102, 4.0, v102
	v_mul_f32_e32 v103, 4.0, v103
	v_fmac_f32_e32 v120, v116, v116
	v_fmac_f32_e32 v99, v106, v106
	v_med3_f32 v102, v102, s87, v227
	v_med3_f32 v103, v103, s87, v227
	v_mov_b32_e32 v116, v167
	v_add_f32_e32 v29, v120, v29
	v_add_f32_e32 v98, v99, v98
	v_cvt_pk_fp8_f32 v116, v102, v103
	v_add_f32_e32 v29, v29, v98
	v_pk_mul_f32 v[98:99], v[8:9], v[104:105]
	v_pk_mul_f32 v[112:113], v[2:3], v[110:111]
	v_mul_f32_e32 v98, 4.0, v98
	v_mul_f32_e32 v99, 4.0, v99
	v_med3_f32 v98, v98, s87, v227
	v_med3_f32 v99, v99, s87, v227
	v_cvt_pk_fp8_f32 v116, v98, v99 op_sel:[0,0,1]
	v_mul_f32_e32 v98, 4.0, v112
	v_mul_f32_e32 v99, 4.0, v113
	v_med3_f32 v98, v98, s87, v227
	v_med3_f32 v99, v99, s87, v227
	v_mov_b32_e32 v117, v167
	v_cvt_pk_fp8_f32 v117, v98, v99
	ds_bpermute_b32 v98, v148, v29
	v_cvt_pk_bf16_f32 v101, v104, v105
	v_pk_mul_f32 v[104:105], v[4:5], v[106:107]
	s_waitcnt lgkmcnt(0)
	v_add_f32_e32 v29, v29, v98
	v_mul_f32_e32 v102, 4.0, v104
	v_med3_f32 v99, v102, s87, v227
	v_mul_f32_e32 v102, 4.0, v105
	ds_bpermute_b32 v98, v149, v29
	v_med3_f32 v102, v102, s87, v227
	v_cvt_pk_fp8_f32 v117, v99, v102 op_sel:[0,0,1]
	v_cvt_pk_bf16_f32 v102, v110, v111
	v_cvt_pk_bf16_f32 v103, v106, v107
	global_store_dwordx4 v[30:31], v[100:103], off offset:256
	global_store_dwordx2 v[108:109], v[116:117], off offset:128
	s_and_saveexec_b64 s[60:61], s[38:39]
	s_cbranch_execz .LBB0_935
	s_waitcnt lgkmcnt(0)
	v_add_f32_e32 v29, v29, v98
	ds_write_b32 v202, v29 offset:192
.LBB0_935:
	s_or_b64 exec, exec, s[60:61]
	s_waitcnt lgkmcnt(0)
	v_add_u32_e32 v98, 0x90, v28
	v_ashrrev_i32_e32 v99, 31, v98
	s_waitcnt vmcnt(4)
	v_lshlrev_b32_e32 v108, 16, v18
	v_and_b32_e32 v109, 0xffff0000, v18
	v_lshlrev_b32_e32 v110, 16, v19
	v_and_b32_e32 v111, 0xffff0000, v19
	v_lshlrev_b64 v[18:19], 11, v[98:99]
	v_lshlrev_b64 v[30:31], 10, v[114:115]
	v_lshl_add_u64 v[18:19], s[26:27], 0, v[18:19]
	v_lshl_add_u64 v[116:117], v[30:31], 0, v[26:27]
	v_lshl_add_u64 v[30:31], v[26:27], 1, v[18:19]
	v_lshlrev_b32_e32 v100, 16, v22
	v_and_b32_e32 v101, 0xffff0000, v22
	v_lshlrev_b32_e32 v102, 16, v23
	v_and_b32_e32 v103, 0xffff0000, v23
	v_lshlrev_b32_e32 v104, 16, v24
	v_and_b32_e32 v105, 0xffff0000, v24
	v_lshlrev_b32_e32 v106, 16, v25
	v_and_b32_e32 v107, 0xffff0000, v25
	v_lshlrev_b32_e32 v112, 16, v20
	v_and_b32_e32 v113, 0xffff0000, v20
	v_lshlrev_b32_e32 v114, 16, v21
	v_and_b32_e32 v115, 0xffff0000, v21
	global_load_dwordx4 v[22:25] v[30:31], off
	global_load_dwordx4 v[18:21] v[30:31], off offset:256
	v_pk_add_f32 v[96:97], v[96:97], v[102:103]
	v_pk_add_f32 v[94:95], v[94:95], v[100:101]
	v_pk_add_f32 v[102:103], v[90:91], v[104:105]
	v_cvt_pk_bf16_f32 v90, v94, v95
	v_pk_add_f32 v[100:101], v[92:93], v[106:107]
	v_cvt_pk_bf16_f32 v91, v96, v97
	v_cvt_pk_bf16_f32 v92, v102, v103
	v_mul_f32_e32 v29, v95, v95
	v_cvt_pk_bf16_f32 v93, v100, v101
	global_store_dwordx4 v[32:33], v[90:93], off
	v_fmac_f32_e32 v29, v94, v94
	v_mul_f32_e32 v104, v101, v101
	v_mul_f32_e32 v90, v97, v97
	v_fmac_f32_e32 v90, v96, v96
	v_add_f32_e32 v29, v29, v90
	v_mul_f32_e32 v90, v103, v103
	v_fmac_f32_e32 v90, v102, v102
	v_pk_mul_f32 v[92:93], v[14:15], v[94:95]
	v_add_f32_e32 v29, v90, v29
	v_pk_mul_f32 v[90:91], v[16:17], v[96:97]
	v_mul_f32_e32 v92, 4.0, v92
	v_mul_f32_e32 v93, 4.0, v93
	v_pk_mul_f32 v[94:95], v[12:13], v[100:101]
	v_med3_f32 v92, v92, s87, v227
	v_med3_f32 v93, v93, s87, v227
	v_mul_f32_e32 v101, 4.0, v90
	v_mov_b32_e32 v90, v167
	v_cvt_pk_fp8_f32 v90, v92, v93
	v_mul_f32_e32 v91, 4.0, v91
	v_pk_mul_f32 v[96:97], v[10:11], v[102:103]
	v_med3_f32 v92, v101, s87, v227
	v_med3_f32 v91, v91, s87, v227
	v_cvt_pk_fp8_f32 v90, v92, v91 op_sel:[0,0,1]
	v_mul_f32_e32 v91, 4.0, v96
	v_med3_f32 v92, v91, s87, v227
	v_mul_f32_e32 v91, 4.0, v97
	v_med3_f32 v93, v91, s87, v227
	v_mov_b32_e32 v91, v167
	v_cvt_pk_fp8_f32 v91, v92, v93
	v_mul_f32_e32 v94, 4.0, v94
	v_mul_f32_e32 v93, 4.0, v95
	v_med3_f32 v92, v94, s87, v227
	v_med3_f32 v93, v93, s87, v227
	v_cvt_pk_fp8_f32 v91, v92, v93 op_sel:[0,0,1]
	v_pk_add_f32 v[88:89], v[88:89], v[110:111]
	v_pk_add_f32 v[86:87], v[86:87], v[108:109]
	v_pk_add_f32 v[94:95], v[82:83], v[112:113]
	v_mul_f32_e32 v82, v87, v87
	v_mul_f32_e32 v83, v89, v89
	v_fmac_f32_e32 v82, v86, v86
	v_fmac_f32_e32 v83, v88, v88
	v_lshl_add_u64 v[92:93], s[34:35], 0, v[116:117]
	v_add_f32_e32 v82, v82, v83
	v_mul_f32_e32 v83, v95, v95
	global_store_dwordx2 v[92:93], v[90:91], off
	v_pk_add_f32 v[90:91], v[84:85], v[114:115]
	v_cvt_pk_bf16_f32 v84, v86, v87
	v_fmac_f32_e32 v83, v94, v94
	v_pk_mul_f32 v[86:87], v[6:7], v[86:87]
	v_add_f32_e32 v82, v83, v82
	v_mul_f32_e32 v83, v91, v91
	v_mul_f32_e32 v86, 4.0, v86
	v_mul_f32_e32 v87, 4.0, v87
	v_fmac_f32_e32 v104, v100, v100
	v_fmac_f32_e32 v83, v90, v90
	v_med3_f32 v86, v86, s87, v227
	v_med3_f32 v87, v87, s87, v227
	v_mov_b32_e32 v100, v167
	v_add_f32_e32 v29, v104, v29
	v_add_f32_e32 v82, v83, v82
	v_cvt_pk_fp8_f32 v100, v86, v87
	v_add_f32_e32 v29, v29, v82
	v_pk_mul_f32 v[82:83], v[8:9], v[88:89]
	v_pk_mul_f32 v[96:97], v[2:3], v[94:95]
	v_mul_f32_e32 v82, 4.0, v82
	v_mul_f32_e32 v83, 4.0, v83
	v_med3_f32 v82, v82, s87, v227
	v_med3_f32 v83, v83, s87, v227
	v_cvt_pk_fp8_f32 v100, v82, v83 op_sel:[0,0,1]
	v_mul_f32_e32 v82, 4.0, v96
	v_mul_f32_e32 v83, 4.0, v97
	v_med3_f32 v82, v82, s87, v227
	v_med3_f32 v83, v83, s87, v227
	v_mov_b32_e32 v101, v167
	v_cvt_pk_fp8_f32 v101, v82, v83
	ds_bpermute_b32 v82, v148, v29
	v_cvt_pk_bf16_f32 v85, v88, v89
	v_pk_mul_f32 v[88:89], v[4:5], v[90:91]
	s_waitcnt lgkmcnt(0)
	v_add_f32_e32 v29, v29, v82
	v_mul_f32_e32 v86, 4.0, v88
	v_med3_f32 v83, v86, s87, v227
	v_mul_f32_e32 v86, 4.0, v89
	ds_bpermute_b32 v82, v149, v29
	v_med3_f32 v86, v86, s87, v227
	v_cvt_pk_fp8_f32 v101, v83, v86 op_sel:[0,0,1]
	v_cvt_pk_bf16_f32 v86, v94, v95
	v_cvt_pk_bf16_f32 v87, v90, v91
	global_store_dwordx4 v[32:33], v[84:87], off offset:256
	global_store_dwordx2 v[92:93], v[100:101], off offset:128
	s_and_saveexec_b64 s[60:61], s[38:39]
	s_cbranch_execz .LBB0_937
	s_waitcnt lgkmcnt(0)
	v_add_f32_e32 v29, v29, v82
	ds_write_b32 v202, v29 offset:512
.LBB0_937:
	s_or_b64 exec, exec, s[60:61]
	s_waitcnt lgkmcnt(0)
	v_add_u32_e32 v82, 0xa0, v28
	v_ashrrev_i32_e32 v83, 31, v82
	s_waitcnt vmcnt(4)
	v_lshlrev_b32_e32 v92, 16, v18
	v_and_b32_e32 v93, 0xffff0000, v18
	v_lshlrev_b32_e32 v94, 16, v19
	v_and_b32_e32 v95, 0xffff0000, v19
	v_lshlrev_b64 v[18:19], 11, v[82:83]
	v_lshlrev_b64 v[32:33], 10, v[98:99]
	v_lshl_add_u64 v[18:19], s[26:27], 0, v[18:19]
	v_lshl_add_u64 v[100:101], v[32:33], 0, v[26:27]
	v_lshl_add_u64 v[32:33], v[26:27], 1, v[18:19]
	v_lshlrev_b32_e32 v84, 16, v22
	v_and_b32_e32 v85, 0xffff0000, v22
	v_lshlrev_b32_e32 v86, 16, v23
	v_and_b32_e32 v87, 0xffff0000, v23
	v_lshlrev_b32_e32 v88, 16, v24
	v_and_b32_e32 v89, 0xffff0000, v24
	v_lshlrev_b32_e32 v90, 16, v25
	v_and_b32_e32 v91, 0xffff0000, v25
	v_lshlrev_b32_e32 v96, 16, v20
	v_and_b32_e32 v97, 0xffff0000, v20
	v_lshlrev_b32_e32 v98, 16, v21
	v_and_b32_e32 v99, 0xffff0000, v21
	global_load_dwordx4 v[22:25] v[32:33], off
	global_load_dwordx4 v[18:21] v[32:33], off offset:256
	v_pk_add_f32 v[80:81], v[80:81], v[86:87]
	v_pk_add_f32 v[78:79], v[78:79], v[84:85]
	v_pk_add_f32 v[86:87], v[74:75], v[88:89]
	v_cvt_pk_bf16_f32 v74, v78, v79
	v_pk_add_f32 v[84:85], v[76:77], v[90:91]
	v_cvt_pk_bf16_f32 v75, v80, v81
	v_cvt_pk_bf16_f32 v76, v86, v87
	v_mul_f32_e32 v29, v79, v79
	v_cvt_pk_bf16_f32 v77, v84, v85
	global_store_dwordx4 v[30:31], v[74:77], off
	v_fmac_f32_e32 v29, v78, v78
	v_mul_f32_e32 v88, v85, v85
	v_mul_f32_e32 v74, v81, v81
	v_fmac_f32_e32 v74, v80, v80
	v_add_f32_e32 v29, v29, v74
	v_mul_f32_e32 v74, v87, v87
	v_fmac_f32_e32 v74, v86, v86
	v_pk_mul_f32 v[76:77], v[14:15], v[78:79]
	v_add_f32_e32 v29, v74, v29
	v_pk_mul_f32 v[74:75], v[16:17], v[80:81]
	v_mul_f32_e32 v76, 4.0, v76
	v_mul_f32_e32 v77, 4.0, v77
	v_pk_mul_f32 v[78:79], v[12:13], v[84:85]
	v_med3_f32 v76, v76, s87, v227
	v_med3_f32 v77, v77, s87, v227
	v_mul_f32_e32 v85, 4.0, v74
	v_mov_b32_e32 v74, v167
	v_cvt_pk_fp8_f32 v74, v76, v77
	v_mul_f32_e32 v75, 4.0, v75
	v_pk_mul_f32 v[80:81], v[10:11], v[86:87]
	v_med3_f32 v76, v85, s87, v227
	v_med3_f32 v75, v75, s87, v227
	v_cvt_pk_fp8_f32 v74, v76, v75 op_sel:[0,0,1]
	v_mul_f32_e32 v75, 4.0, v80
	v_med3_f32 v76, v75, s87, v227
	v_mul_f32_e32 v75, 4.0, v81
	v_med3_f32 v77, v75, s87, v227
	v_mov_b32_e32 v75, v167
	v_cvt_pk_fp8_f32 v75, v76, v77
	v_mul_f32_e32 v78, 4.0, v78
	v_mul_f32_e32 v77, 4.0, v79
	v_med3_f32 v76, v78, s87, v227
	v_med3_f32 v77, v77, s87, v227
	v_cvt_pk_fp8_f32 v75, v76, v77 op_sel:[0,0,1]
	v_pk_add_f32 v[72:73], v[72:73], v[94:95]
	v_pk_add_f32 v[70:71], v[70:71], v[92:93]
	v_pk_add_f32 v[78:79], v[66:67], v[96:97]
	v_mul_f32_e32 v66, v71, v71
	v_mul_f32_e32 v67, v73, v73
	v_fmac_f32_e32 v66, v70, v70
	v_fmac_f32_e32 v67, v72, v72
	v_lshl_add_u64 v[76:77], s[34:35], 0, v[100:101]
	v_add_f32_e32 v66, v66, v67
	v_mul_f32_e32 v67, v79, v79
	global_store_dwordx2 v[76:77], v[74:75], off
	v_pk_add_f32 v[74:75], v[68:69], v[98:99]
	v_cvt_pk_bf16_f32 v68, v70, v71
	v_fmac_f32_e32 v67, v78, v78
	v_pk_mul_f32 v[70:71], v[6:7], v[70:71]
	v_add_f32_e32 v66, v67, v66
	v_mul_f32_e32 v67, v75, v75
	v_mul_f32_e32 v70, 4.0, v70
	v_mul_f32_e32 v71, 4.0, v71
	v_fmac_f32_e32 v88, v84, v84
	v_fmac_f32_e32 v67, v74, v74
	v_med3_f32 v70, v70, s87, v227
	v_med3_f32 v71, v71, s87, v227
	v_mov_b32_e32 v84, v167
	v_add_f32_e32 v29, v88, v29
	v_add_f32_e32 v66, v67, v66
	v_cvt_pk_fp8_f32 v84, v70, v71
	v_add_f32_e32 v29, v29, v66
	v_pk_mul_f32 v[66:67], v[8:9], v[72:73]
	v_pk_mul_f32 v[80:81], v[2:3], v[78:79]
	v_mul_f32_e32 v66, 4.0, v66
	v_mul_f32_e32 v67, 4.0, v67
	v_med3_f32 v66, v66, s87, v227
	v_med3_f32 v67, v67, s87, v227
	v_cvt_pk_fp8_f32 v84, v66, v67 op_sel:[0,0,1]
	v_mul_f32_e32 v66, 4.0, v80
	v_mul_f32_e32 v67, 4.0, v81
	v_med3_f32 v66, v66, s87, v227
	v_med3_f32 v67, v67, s87, v227
	v_mov_b32_e32 v85, v167
	v_cvt_pk_fp8_f32 v85, v66, v67
	ds_bpermute_b32 v66, v148, v29
	v_cvt_pk_bf16_f32 v69, v72, v73
	v_pk_mul_f32 v[72:73], v[4:5], v[74:75]
	s_waitcnt lgkmcnt(0)
	v_add_f32_e32 v29, v29, v66
	v_mul_f32_e32 v70, 4.0, v72
	v_med3_f32 v67, v70, s87, v227
	v_mul_f32_e32 v70, 4.0, v73
	ds_bpermute_b32 v66, v149, v29
	v_med3_f32 v70, v70, s87, v227
	v_cvt_pk_fp8_f32 v85, v67, v70 op_sel:[0,0,1]
	v_cvt_pk_bf16_f32 v70, v78, v79
	v_cvt_pk_bf16_f32 v71, v74, v75
	global_store_dwordx4 v[30:31], v[68:71], off offset:256
	global_store_dwordx2 v[76:77], v[84:85], off offset:128
	s_and_saveexec_b64 s[60:61], s[38:39]
	s_cbranch_execz .LBB0_939
	s_waitcnt lgkmcnt(0)
	v_add_f32_e32 v29, v29, v66
	ds_write_b32 v202, v29 offset:576
.LBB0_939:
	s_or_b64 exec, exec, s[60:61]
	v_lshlrev_b64 v[30:31], 10, v[82:83]
	v_lshl_add_u64 v[82:83], v[30:31], 0, v[26:27]
	v_add_u32_e32 v30, 0xb0, v28
	v_ashrrev_i32_e32 v31, 31, v30
	s_waitcnt vmcnt(4)
	v_lshlrev_b32_e32 v74, 16, v18
	v_and_b32_e32 v75, 0xffff0000, v18
	v_lshlrev_b32_e32 v76, 16, v19
	v_and_b32_e32 v77, 0xffff0000, v19
	v_lshlrev_b64 v[18:19], 11, v[30:31]
	v_lshl_add_u64 v[18:19], s[26:27], 0, v[18:19]
	v_lshl_add_u64 v[28:29], v[26:27], 1, v[18:19]
	s_waitcnt lgkmcnt(0)
	v_lshlrev_b32_e32 v66, 16, v22
	v_and_b32_e32 v67, 0xffff0000, v22
	v_lshlrev_b32_e32 v68, 16, v23
	v_and_b32_e32 v69, 0xffff0000, v23
	v_lshlrev_b32_e32 v70, 16, v24
	v_and_b32_e32 v71, 0xffff0000, v24
	v_lshlrev_b32_e32 v72, 16, v25
	v_and_b32_e32 v73, 0xffff0000, v25
	v_lshlrev_b32_e32 v78, 16, v20
	v_and_b32_e32 v79, 0xffff0000, v20
	v_lshlrev_b32_e32 v80, 16, v21
	v_and_b32_e32 v81, 0xffff0000, v21
	global_load_dwordx4 v[18:21] v[28:29], off
	global_load_dwordx4 v[22:25] v[28:29], off offset:256
	v_pk_add_f32 v[64:65], v[64:65], v[68:69]
	v_pk_add_f32 v[62:63], v[62:63], v[66:67]
	v_pk_add_f32 v[68:69], v[58:59], v[70:71]
	v_cvt_pk_bf16_f32 v58, v62, v63
	v_cvt_pk_bf16_f32 v59, v64, v65
	v_pk_add_f32 v[66:67], v[60:61], v[72:73]
	v_cvt_pk_bf16_f32 v60, v68, v69
	v_pk_add_f32 v[56:57], v[56:57], v[76:77]
	v_cvt_pk_bf16_f32 v61, v66, v67
	global_store_dwordx4 v[32:33], v[58:61], off
	v_mul_f32_e32 v71, v67, v67
	v_pk_add_f32 v[54:55], v[54:55], v[74:75]
	v_mul_f32_e32 v58, v63, v63
	v_mul_f32_e32 v59, v65, v65
	v_fmac_f32_e32 v58, v62, v62
	v_fmac_f32_e32 v59, v64, v64
	v_add_f32_e32 v58, v58, v59
	v_mul_f32_e32 v59, v69, v69
	v_fmac_f32_e32 v59, v68, v68
	v_pk_mul_f32 v[60:61], v[14:15], v[62:63]
	v_add_f32_e32 v70, v59, v58
	v_pk_mul_f32 v[58:59], v[16:17], v[64:65]
	v_mul_f32_e32 v60, 4.0, v60
	v_mul_f32_e32 v61, 4.0, v61
	v_pk_mul_f32 v[62:63], v[12:13], v[66:67]
	v_med3_f32 v60, v60, s87, v227
	v_med3_f32 v61, v61, s87, v227
	v_mul_f32_e32 v67, 4.0, v58
	v_mov_b32_e32 v58, v167
	v_cvt_pk_fp8_f32 v58, v60, v61
	v_mul_f32_e32 v59, 4.0, v59
	v_pk_mul_f32 v[64:65], v[10:11], v[68:69]
	v_med3_f32 v60, v67, s87, v227
	v_med3_f32 v59, v59, s87, v227
	v_cvt_pk_fp8_f32 v58, v60, v59 op_sel:[0,0,1]
	v_mul_f32_e32 v59, 4.0, v64
	v_med3_f32 v60, v59, s87, v227
	v_mul_f32_e32 v59, 4.0, v65
	v_med3_f32 v61, v59, s87, v227
	v_mov_b32_e32 v59, v167
	v_cvt_pk_fp8_f32 v59, v60, v61
	v_mul_f32_e32 v62, 4.0, v62
	v_mul_f32_e32 v61, 4.0, v63
	v_med3_f32 v60, v62, s87, v227
	v_med3_f32 v61, v61, s87, v227
	v_cvt_pk_fp8_f32 v59, v60, v61 op_sel:[0,0,1]
	v_pk_add_f32 v[62:63], v[50:51], v[78:79]
	v_mul_f32_e32 v50, v55, v55
	v_mul_f32_e32 v51, v57, v57
	v_fmac_f32_e32 v50, v54, v54
	v_fmac_f32_e32 v51, v56, v56
	v_lshl_add_u64 v[60:61], s[34:35], 0, v[82:83]
	v_add_f32_e32 v50, v50, v51
	v_mul_f32_e32 v51, v63, v63
	global_store_dwordx2 v[60:61], v[58:59], off
	v_pk_add_f32 v[58:59], v[52:53], v[80:81]
	v_cvt_pk_bf16_f32 v52, v54, v55
	v_fmac_f32_e32 v51, v62, v62
	v_pk_mul_f32 v[54:55], v[6:7], v[54:55]
	v_add_f32_e32 v50, v51, v50
	v_mul_f32_e32 v51, v59, v59
	v_mul_f32_e32 v54, 4.0, v54
	v_mul_f32_e32 v55, 4.0, v55
	v_fmac_f32_e32 v71, v66, v66
	v_fmac_f32_e32 v51, v58, v58
	v_med3_f32 v54, v54, s87, v227
	v_med3_f32 v55, v55, s87, v227
	v_mov_b32_e32 v66, v167
	v_add_f32_e32 v64, v71, v70
	v_add_f32_e32 v50, v51, v50
	v_cvt_pk_fp8_f32 v66, v54, v55
	v_add_f32_e32 v68, v64, v50
	v_pk_mul_f32 v[50:51], v[8:9], v[56:57]
	v_pk_mul_f32 v[64:65], v[2:3], v[62:63]
	v_mul_f32_e32 v50, 4.0, v50
	v_mul_f32_e32 v51, 4.0, v51
	v_med3_f32 v50, v50, s87, v227
	v_med3_f32 v51, v51, s87, v227
	v_cvt_pk_fp8_f32 v66, v50, v51 op_sel:[0,0,1]
	v_mul_f32_e32 v50, 4.0, v64
	v_mul_f32_e32 v51, 4.0, v65
	v_med3_f32 v50, v50, s87, v227
	v_med3_f32 v51, v51, s87, v227
	v_mov_b32_e32 v67, v167
	v_cvt_pk_fp8_f32 v67, v50, v51
	ds_bpermute_b32 v50, v148, v68
	v_cvt_pk_bf16_f32 v53, v56, v57
	v_pk_mul_f32 v[56:57], v[4:5], v[58:59]
	s_waitcnt lgkmcnt(0)
	v_add_f32_e32 v50, v68, v50
	v_mul_f32_e32 v54, 4.0, v56
	v_med3_f32 v51, v54, s87, v227
	v_mul_f32_e32 v54, 4.0, v57
	v_med3_f32 v54, v54, s87, v227
	v_cvt_pk_fp8_f32 v67, v51, v54 op_sel:[0,0,1]
	ds_bpermute_b32 v51, v149, v50
	v_cvt_pk_bf16_f32 v54, v62, v63
	v_cvt_pk_bf16_f32 v55, v58, v59
	global_store_dwordx4 v[32:33], v[52:55], off offset:256
	global_store_dwordx2 v[60:61], v[66:67], off offset:128
	s_and_saveexec_b64 s[60:61], s[38:39]
	s_cbranch_execz .LBB0_941
	s_waitcnt lgkmcnt(0)
	v_add_f32_e32 v32, v50, v51
	ds_write_b32 v202, v32 offset:640
.LBB0_941:
	s_or_b64 exec, exec, s[60:61]
	s_waitcnt vmcnt(4)
	v_lshlrev_b32_e32 v52, 16, v18
	v_and_b32_e32 v53, 0xffff0000, v18
	v_lshlrev_b64 v[30:31], 10, v[30:31]
	v_pk_add_f32 v[46:47], v[46:47], v[52:53]
	v_lshl_add_u64 v[26:27], v[30:31], 0, v[26:27]
	v_lshlrev_b32_e32 v30, 16, v20
	v_and_b32_e32 v31, 0xffff0000, v20
	v_lshlrev_b32_e32 v20, 16, v21
	v_and_b32_e32 v21, 0xffff0000, v21
	v_lshlrev_b32_e32 v18, 16, v19
	v_and_b32_e32 v19, 0xffff0000, v19
	v_pk_mul_f32 v[14:15], v[14:15], v[46:47]
	v_pk_add_f32 v[48:49], v[48:49], v[18:19]
	v_pk_add_f32 v[44:45], v[44:45], v[20:21]
	v_pk_add_f32 v[30:31], v[42:43], v[30:31]
	v_cvt_pk_bf16_f32 v18, v46, v47
	v_cvt_pk_bf16_f32 v19, v48, v49
	v_mul_f32_e32 v14, 4.0, v14
	v_cvt_pk_bf16_f32 v20, v30, v31
	v_cvt_pk_bf16_f32 v21, v44, v45
	global_store_dwordx4 v[28:29], v[18:21], off
	v_pk_mul_f32 v[16:17], v[16:17], v[48:49]
	v_pk_mul_f32 v[10:11], v[10:11], v[30:31]
	v_med3_f32 v20, v14, s87, v227
	v_mul_f32_e32 v14, 4.0, v15
	v_med3_f32 v15, v14, s87, v227
	v_mov_b32_e32 v14, v167
	v_cvt_pk_fp8_f32 v14, v20, v15
	v_mul_f32_e32 v16, 4.0, v16
	v_med3_f32 v15, v16, s87, v227
	v_mul_f32_e32 v16, 4.0, v17
	v_med3_f32 v16, v16, s87, v227
	v_mul_f32_e32 v10, 4.0, v10
	v_mul_f32_e32 v11, 4.0, v11
	v_cvt_pk_fp8_f32 v14, v15, v16 op_sel:[0,0,1]
	v_med3_f32 v10, v10, s87, v227
	v_med3_f32 v11, v11, s87, v227
	v_mov_b32_e32 v15, v167
	v_cvt_pk_fp8_f32 v15, v10, v11
	v_pk_mul_f32 v[12:13], v[12:13], v[44:45]
	v_lshlrev_b32_e32 v32, 16, v22
	v_mul_f32_e32 v12, 4.0, v12
	v_mul_f32_e32 v11, 4.0, v13
	v_med3_f32 v10, v12, s87, v227
	v_med3_f32 v11, v11, s87, v227
	v_cvt_pk_fp8_f32 v15, v10, v11 op_sel:[0,0,1]
	v_and_b32_e32 v33, 0xffff0000, v22
	v_mul_f32_e32 v18, v47, v47
	v_mul_f32_e32 v19, v49, v49
	v_lshl_add_u64 v[16:17], s[34:35], 0, v[26:27]
	v_lshlrev_b32_e32 v22, 16, v23
	v_and_b32_e32 v23, 0xffff0000, v23
	v_fmac_f32_e32 v18, v46, v46
	v_fmac_f32_e32 v19, v48, v48
	global_store_dwordx2 v[16:17], v[14:15], off
	v_pk_add_f32 v[14:15], v[38:39], v[32:33]
	v_add_f32_e32 v18, v18, v19
	v_mul_f32_e32 v19, v31, v31
	v_pk_add_f32 v[12:13], v[40:41], v[22:23]
	v_pk_mul_f32 v[6:7], v[6:7], v[14:15]
	v_lshlrev_b32_e32 v50, 16, v24
	s_waitcnt lgkmcnt(0)
	v_and_b32_e32 v51, 0xffff0000, v24
	v_fmac_f32_e32 v19, v30, v30
	v_mul_f32_e32 v22, v15, v15
	v_mul_f32_e32 v23, v13, v13
	v_mul_f32_e32 v6, 4.0, v6
	v_add_f32_e32 v18, v19, v18
	v_mul_f32_e32 v19, v45, v45
	v_pk_add_f32 v[20:21], v[34:35], v[50:51]
	v_cvt_pk_bf16_f32 v10, v14, v15
	v_cvt_pk_bf16_f32 v11, v12, v13
	v_fmac_f32_e32 v22, v14, v14
	v_fmac_f32_e32 v23, v12, v12
	v_pk_mul_f32 v[8:9], v[8:9], v[12:13]
	v_med3_f32 v12, v6, s87, v227
	v_mul_f32_e32 v6, 4.0, v7
	v_lshlrev_b32_e32 v24, 16, v25
	v_and_b32_e32 v25, 0xffff0000, v25
	v_fmac_f32_e32 v19, v44, v44
	v_add_f32_e32 v22, v22, v23
	v_mul_f32_e32 v23, v21, v21
	v_med3_f32 v7, v6, s87, v227
	v_mov_b32_e32 v6, v167
	v_add_f32_e32 v30, v19, v18
	v_pk_add_f32 v[18:19], v[36:37], v[24:25]
	v_fmac_f32_e32 v23, v20, v20
	v_cvt_pk_fp8_f32 v6, v12, v7
	v_add_f32_e32 v22, v23, v22
	v_mul_f32_e32 v23, v19, v19
	v_mul_f32_e32 v8, 4.0, v8
	v_fmac_f32_e32 v23, v18, v18
	v_pk_mul_f32 v[2:3], v[2:3], v[20:21]
	v_med3_f32 v7, v8, s87, v227
	v_mul_f32_e32 v8, 4.0, v9
	v_add_f32_e32 v22, v23, v22
	v_med3_f32 v8, v8, s87, v227
	v_mul_f32_e32 v2, 4.0, v2
	v_mul_f32_e32 v3, 4.0, v3
	v_add_f32_e32 v22, v30, v22
	v_cvt_pk_fp8_f32 v6, v7, v8 op_sel:[0,0,1]
	v_med3_f32 v2, v2, s87, v227
	v_med3_f32 v3, v3, s87, v227
	v_mov_b32_e32 v7, v167
	v_cvt_pk_fp8_f32 v7, v2, v3
	ds_bpermute_b32 v2, v148, v22
	v_pk_mul_f32 v[4:5], v[4:5], v[18:19]
	v_cvt_pk_bf16_f32 v12, v20, v21
	v_cvt_pk_bf16_f32 v13, v18, v19
	s_waitcnt lgkmcnt(0)
	v_add_f32_e32 v2, v22, v2
	v_mul_f32_e32 v4, 4.0, v4
	v_med3_f32 v3, v4, s87, v227
	v_mul_f32_e32 v4, 4.0, v5
	v_med3_f32 v4, v4, s87, v227
	v_cvt_pk_fp8_f32 v7, v3, v4 op_sel:[0,0,1]
	ds_bpermute_b32 v3, v149, v2
	global_store_dwordx4 v[28:29], v[10:13], off offset:256
	global_store_dwordx2 v[16:17], v[6:7], off offset:128
	s_and_saveexec_b64 s[60:61], s[38:39]
	s_cbranch_execz .LBB0_943
	s_waitcnt lgkmcnt(0)
	v_add_f32_e32 v2, v2, v3
	ds_write_b32 v202, v2 offset:704

.LBB0_1014:
	s_ashr_i32 s27, s26, 31
	s_lshl_b64 s[0:1], s[26:27], 18
	s_add_u32 s30, s90, s0
	s_addc_u32 s31, s91, s1
	s_ashr_i32 s65, s64, 31
	s_lshl_b64 s[0:1], s[64:65], 18
	s_add_u32 s34, s76, s0
	s_addc_u32 s35, s77, s1
	s_andn2_b64 vcc, exec, s[50:51]
	s_cbranch_vccnz .LBB0_1078
	v_lshl_add_u32 v2, s36, 8, v220
	v_ashrrev_i32_e32 v3, 31, v2
	v_lshl_add_u64 v[4:5], v[2:3], 2, v[186:187]
	global_load_dword v172, v[4:5], off
	global_load_dword v173, v[4:5], off offset:64
	global_load_dword v174, v[4:5], off offset:128
	global_load_dword v175, v[4:5], off offset:192
	global_load_dword v176, v[4:5], off offset:512
	global_load_dword v177, v[4:5], off offset:576
	global_load_dword v223, v[4:5], off offset:640
	global_load_dword v232, v[4:5], off offset:704
	s_and_b64 s[0:1], s[28:29], exec
	s_cselect_b32 s0, s31, s39
	s_cselect_b32 s1, s30, s38
	s_cselect_b32 s8, s35, s41
	s_cselect_b32 s11, s34, s40
	s_add_u32 s16, s40, 0x100
	s_addc_u32 s19, s41, 0
	s_add_u32 s38, s38, 0x20080
	v_mov_b32_e32 v114, 0
	v_mov_b32_e32 v1, 0x3ecc95a3
	s_addc_u32 s39, s39, 0
	s_mov_b32 s37, 0
	v_mov_b32_e32 v115, v114
	v_mov_b32_e32 v116, v114
	v_mov_b32_e32 v117, v114
	v_mov_b32_e32 v118, v114
	v_mov_b32_e32 v119, v114
	v_mov_b32_e32 v120, v114
	v_mov_b32_e32 v121, v114
	v_mov_b32_e32 v122, v114
	v_mov_b32_e32 v123, v114
	v_mov_b32_e32 v124, v114
	v_mov_b32_e32 v125, v114
	v_mov_b32_e32 v126, v114
	v_mov_b32_e32 v127, v114
	v_mov_b32_e32 v128, v114
	v_mov_b32_e32 v129, v114
	v_mov_b32_e32 v34, v114
	v_mov_b32_e32 v35, v114
	v_mov_b32_e32 v36, v114
	v_mov_b32_e32 v37, v114
	v_mov_b32_e32 v38, v114
	v_mov_b32_e32 v39, v114
	v_mov_b32_e32 v40, v114
	v_mov_b32_e32 v41, v114
	v_mov_b32_e32 v42, v114
	v_mov_b32_e32 v43, v114
	v_mov_b32_e32 v44, v114
	v_mov_b32_e32 v45, v114
	v_mov_b32_e32 v46, v114
	v_mov_b32_e32 v47, v114
	v_mov_b32_e32 v48, v114
	v_mov_b32_e32 v49, v114
	v_mov_b32_e32 v50, v114
	v_mov_b32_e32 v51, v114
	v_mov_b32_e32 v52, v114
	v_mov_b32_e32 v53, v114
	v_mov_b32_e32 v54, v114
	v_mov_b32_e32 v55, v114
	v_mov_b32_e32 v56, v114
	v_mov_b32_e32 v57, v114
	v_mov_b32_e32 v58, v114
	v_mov_b32_e32 v59, v114
	v_mov_b32_e32 v60, v114
	v_mov_b32_e32 v61, v114
	v_mov_b32_e32 v62, v114
	v_mov_b32_e32 v63, v114
	v_mov_b32_e32 v64, v114
	v_mov_b32_e32 v65, v114
	v_mov_b32_e32 v130, v114
	v_mov_b32_e32 v131, v114
	v_mov_b32_e32 v132, v114
	v_mov_b32_e32 v133, v114
	v_mov_b32_e32 v134, v114
	v_mov_b32_e32 v135, v114
	v_mov_b32_e32 v136, v114
	v_mov_b32_e32 v137, v114
	v_mov_b32_e32 v138, v114
	v_mov_b32_e32 v139, v114
	v_mov_b32_e32 v140, v114
	v_mov_b32_e32 v141, v114
	v_mov_b32_e32 v142, v114
	v_mov_b32_e32 v143, v114
	v_mov_b32_e32 v144, v114
	v_mov_b32_e32 v145, v114
	v_mov_b32_e32 v146, v114
	v_mov_b32_e32 v147, v114
	v_mov_b32_e32 v148, v114
	v_mov_b32_e32 v149, v114
	v_mov_b32_e32 v150, v114
	v_mov_b32_e32 v151, v114
	v_mov_b32_e32 v152, v114
	v_mov_b32_e32 v153, v114
	v_mov_b32_e32 v154, v114
	v_mov_b32_e32 v155, v114
	v_mov_b32_e32 v156, v114
	v_mov_b32_e32 v157, v114
	v_mov_b32_e32 v158, v114
	v_mov_b32_e32 v159, v114
	v_mov_b32_e32 v160, v114
	v_mov_b32_e32 v161, v114
	v_mov_b32_e32 v66, v114
	v_mov_b32_e32 v67, v114
	v_mov_b32_e32 v68, v114
	v_mov_b32_e32 v69, v114
	v_mov_b32_e32 v70, v114
	v_mov_b32_e32 v71, v114
	v_mov_b32_e32 v72, v114
	v_mov_b32_e32 v73, v114
	v_mov_b32_e32 v74, v114
	v_mov_b32_e32 v75, v114
	v_mov_b32_e32 v76, v114
	v_mov_b32_e32 v77, v114
	v_mov_b32_e32 v78, v114
	v_mov_b32_e32 v79, v114
	v_mov_b32_e32 v80, v114
	v_mov_b32_e32 v81, v114
	v_mov_b32_e32 v82, v114
	v_mov_b32_e32 v83, v114
	v_mov_b32_e32 v84, v114
	v_mov_b32_e32 v85, v114
	v_mov_b32_e32 v86, v114
	v_mov_b32_e32 v87, v114
	v_mov_b32_e32 v88, v114
	v_mov_b32_e32 v89, v114
	v_mov_b32_e32 v90, v114
	v_mov_b32_e32 v91, v114
	v_mov_b32_e32 v92, v114
	v_mov_b32_e32 v93, v114
	v_mov_b32_e32 v94, v114
	v_mov_b32_e32 v95, v114
	v_mov_b32_e32 v96, v114
	v_mov_b32_e32 v97, v114
	v_mov_b32_e32 v110, v114
	v_mov_b32_e32 v111, v114
	v_mov_b32_e32 v112, v114
	v_mov_b32_e32 v113, v114
	v_mov_b32_e32 v106, v114
	v_mov_b32_e32 v107, v114
	v_mov_b32_e32 v108, v114
	v_mov_b32_e32 v109, v114
	v_mov_b32_e32 v102, v114
	v_mov_b32_e32 v103, v114
	v_mov_b32_e32 v104, v114
	v_mov_b32_e32 v105, v114
	v_mov_b32_e32 v98, v114
	v_mov_b32_e32 v99, v114
	v_mov_b32_e32 v100, v114
	v_mov_b32_e32 v101, v114

.LBB0_1019:
	v_lshl_add_u32 v194, s36, 8, v220
	s_nop 15
	s_nop 7
	v_and_b32_e32 v11, 64, v231
	v_ashrrev_i32_e32 v195, 31, v194
	v_xor_b32_e32 v10, 16, v231
	v_add_u32_e32 v11, 64, v11
	v_cmp_lt_i32_e32 vcc, v10, v11
	s_ashr_i32 s68, s18, 2
	s_mov_b64 s[36:37], -1
	v_cndmask_b32_e32 v10, v231, v10, vcc
	v_lshlrev_b32_e32 v19, 2, v10
	v_xor_b32_e32 v10, 32, v231
	v_cmp_lt_i32_e32 vcc, v10, v11
	s_nop 1
	v_cndmask_b32_e32 v10, v231, v10, vcc
	v_lshlrev_b32_e32 v21, 2, v10
	ds_bpermute_b32 v2, v19, v172
	ds_bpermute_b32 v3, v19, v173
	ds_bpermute_b32 v4, v19, v174
	ds_bpermute_b32 v5, v19, v175
	ds_bpermute_b32 v6, v19, v176
	ds_bpermute_b32 v7, v19, v177
	ds_bpermute_b32 v8, v19, v223
	ds_bpermute_b32 v9, v19, v232
	s_waitcnt lgkmcnt(7)
	v_add_f32_e32 v172, v172, v2
	ds_bpermute_b32 v2, v21, v172
	s_waitcnt lgkmcnt(7)
	v_add_f32_e32 v173, v173, v3
	ds_bpermute_b32 v3, v21, v173
	s_waitcnt lgkmcnt(7)
	v_add_f32_e32 v174, v174, v4
	ds_bpermute_b32 v4, v21, v174
	s_waitcnt lgkmcnt(7)
	v_add_f32_e32 v175, v175, v5
	ds_bpermute_b32 v5, v21, v175
	s_waitcnt lgkmcnt(7)
	v_add_f32_e32 v176, v176, v6
	ds_bpermute_b32 v6, v21, v176
	s_waitcnt lgkmcnt(7)
	v_add_f32_e32 v177, v177, v7
	ds_bpermute_b32 v7, v21, v177
	s_waitcnt lgkmcnt(7)
	v_add_f32_e32 v223, v223, v8
	ds_bpermute_b32 v8, v21, v223
	s_waitcnt lgkmcnt(7)
	v_add_f32_e32 v232, v232, v9
	ds_bpermute_b32 v9, v21, v232
	s_waitcnt lgkmcnt(7)
	v_add_f32_e32 v172, v172, v2
	v_fmamk_f32 v172, v172, 0x3a800000, v224
	s_waitcnt lgkmcnt(6)
	v_add_f32_e32 v173, v173, v3
	v_fmamk_f32 v173, v173, 0x3a800000, v224
	s_waitcnt lgkmcnt(5)
	v_add_f32_e32 v174, v174, v4
	v_fmamk_f32 v174, v174, 0x3a800000, v224
	s_waitcnt lgkmcnt(4)
	v_add_f32_e32 v175, v175, v5
	v_fmamk_f32 v175, v175, 0x3a800000, v224
	s_waitcnt lgkmcnt(3)
	v_add_f32_e32 v176, v176, v6
	v_fmamk_f32 v176, v176, 0x3a800000, v224
	s_waitcnt lgkmcnt(2)
	v_add_f32_e32 v177, v177, v7
	v_fmamk_f32 v177, v177, 0x3a800000, v224
	s_waitcnt lgkmcnt(1)
	v_add_f32_e32 v223, v223, v8
	v_fmamk_f32 v223, v223, 0x3a800000, v224
	s_waitcnt lgkmcnt(0)
	v_add_f32_e32 v232, v232, v9
	v_fmamk_f32 v232, v232, 0x3a800000, v224
	v_rsq_f32_e32 v32, v172
	v_rsq_f32_e32 v30, v173
	v_rsq_f32_e32 v28, v174
	v_rsq_f32_e32 v26, v175
	v_rsq_f32_e32 v24, v176
	v_rsq_f32_e32 v22, v177
	v_rsq_f32_e32 v20, v223
	v_rsq_f32_e32 v18, v232
	s_cmp_lg_u32 s68, 4
	s_cbranch_scc1 .LBB0_1022
	s_and_b64 vcc, exec, s[36:37]
	s_cbranch_vccnz .LBB0_1073

.LBB0_1190:
	v_readlane_b32 s10, v254, 0
	s_cmp_le_i32 s10, s0
	s_cselect_b64 s[0:1], -1, 0
	s_and_b64 s[18:19], s[0:1], s[26:27]
	s_andn2_b64 vcc, exec, s[18:19]
	v_readlane_b32 s11, v254, 1
	s_cbranch_vccnz .LBB0_1368
	s_mov_b32 s100, m0
	v_readlane_b32 s12, v254, 2
	v_readlane_b32 s14, v254, 4
	v_readlane_b32 s15, v254, 5
	s_waitcnt lgkmcnt(0)
	s_mov_b64 s[36:37], s[14:15]
	s_mov_b32 s0, s2
	v_readlane_b32 s13, v254, 3
	s_mov_b64 s[0:1], s[12:13]
	v_mov_b32_e32 v178, v0
	s_mov_b32 s28, 13
	v_and_b32_e32 v169, 63, v178
	v_cmp_gt_u32_e32 vcc, 16, v169
	v_mov_b32_e32 v185, 0x63
	s_and_saveexec_b64 s[26:27], vcc
	s_cbranch_execz .LBB0_1253
	v_readlane_b32 s0, v254, 63
	v_readlane_b32 s1, v255, 0
	s_ashr_i32 s29, s28, 31
	s_lshl_b32 s66, s0, 4
	s_lshl_b64 s[0:1], s[28:29], 3
	s_add_u32 s0, s94, s0
	s_addc_u32 s1, s95, s1
	s_load_dwordx2 s[0:1], s[0:1], 0x0
	s_lshl_b64 s[10:11], s[66:67], 2
	v_lshlrev_b32_e32 v166, 2, v169
	s_waitcnt lgkmcnt(0)
	s_add_u32 s28, s0, s10
	s_addc_u32 s29, s1, s11
	s_waitcnt vmcnt(0)
	v_lshl_add_u64 v[2:3], s[28:29], 0, v[166:167]
	v_mov_b64_e32 v[4:5], s[28:29]
	flat_load_dword v2, v[2:3]
	s_nop 0
	flat_load_dword v5, v[4:5]
	v_mov_b32_e32 v3, 1
	v_mov_b32_e32 v4, 1
	s_waitcnt vmcnt(0) lgkmcnt(0)
	v_cmp_ngt_f32_e32 vcc, v5, v2
	s_and_saveexec_b64 s[30:31], vcc
	s_cbranch_execz .LBB0_1196
	v_cmp_eq_f32_e32 vcc, v5, v2
	v_mov_b32_e32 v4, 0
	s_and_saveexec_b64 s[34:35], vcc
	v_cmp_ne_u32_e32 vcc, 0, v169
	s_nop 1
	v_cndmask_b32_e64 v4, 0, 1, vcc
	s_or_b64 exec, exec, s[34:35]

.LBB0_1317:
	v_add_f32_e32 v193, 0, v154
	s_or_b32 s44, s60, 1
	s_cmp_ge_i32 s44, s71
	s_cbranch_scc1 .LBB0_1360
	s_and_b64 s[52:53], s[52:53], exec
	s_cselect_b32 s60, 3, 2
	s_ashr_i32 s45, s44, 31
	s_lshl_b64 s[52:53], s[44:45], 17
	s_add_u32 s45, s52, s46
	s_addc_u32 s59, s53, s47
	s_lshl_b64 s[52:53], s[54:55], 1
	s_add_u32 s52, s45, s52
	s_addc_u32 s53, s59, s53
	s_lshl_b32 s45, s24, 15
	s_and_b32 s45, s45, 0x18000
	v_lshl_add_u32 v66, s58, 6, v246
	v_lshl_or_b32 v166, v247, 1, s45
	v_subrev_u32_e32 v195, s75, v66
	v_lshl_add_u64 v[66:67], s[52:53], 0, v[166:167]
	s_add_i32 s52, s16, s73
	s_add_i32 s54, s58, 4
	s_ashr_i32 s53, s52, 31
	s_ashr_i32 s55, s54, 31
	s_lshl_b64 s[52:53], s[52:53], 18
	s_lshl_b64 s[58:59], s[54:55], 11
	s_add_u32 s45, s52, s58
	s_addc_u32 s53, s53, s59
	s_and_b32 s52, s74, 16
	s_or_b32 s52, s45, s52
	v_lshl_add_u64 v[220:221], v[188:189], 0, s[52:53]
	s_lshl_b64 s[52:53], s[54:55], 17
	s_add_u32 s45, s52, s46
	s_addc_u32 s52, s53, s47
	s_lshl_b64 s[50:51], s[50:51], 1
	s_add_u32 s50, s45, s50
	s_addc_u32 s51, s52, s51
	v_lshl_add_u64 v[218:219], v[208:209], 0, v[66:67]
	v_lshl_add_u64 v[222:223], v[210:211], 0, s[50:51]
	s_mov_b32 s100, m0
.LBB0_1319:
	s_add_i32 s45, s44, -2
	s_mul_hi_i32 s50, s45, 0x55555556
	s_mul_i32 s50, s50, 3
	s_sub_i32 s45, s45, s50
	v_lshl_add_u32 v162, s45, 13, v240
	ds_read_b64_tr_b16 v[142:143], v162 offset:40960
	ds_read_b64_tr_b16 v[144:145], v162 offset:41472
	s_add_i32 s45, s44, -1
	v_mfma_f32_32x32x16_bf16 v[82:97], v[138:141], v[98:101], 0
	v_add_f32_e32 v66, v50, v51
	v_add_f32_e32 v67, v52, v53
	v_add_f32_e32 v66, v66, v67
	v_add_f32_e32 v66, 0, v66
	v_cvt_pk_bf16_f32 v138, v50, v51
	v_cvt_pk_bf16_f32 v139, v52, v53
	ds_read_b64_tr_b16 v[146:147], v162 offset:45056
	ds_read_b64_tr_b16 v[148:149], v162 offset:45568
	v_add_f32_e32 v50, v54, v55
	v_add_f32_e32 v51, v56, v57
	v_add_f32_e32 v50, v50, v51
	v_add_f32_e32 v50, v50, v66
	v_mfma_f32_32x32x16_bf16 v[66:81], v[130:133], v[98:101], 0
	v_cvt_pk_bf16_f32 v140, v54, v55
	v_cvt_pk_bf16_f32 v141, v56, v57
	s_and_b32 s50, s45, 3
	s_mulk_i32 s50, 0x2800
	v_add_u32_e32 v150, s50, v238
	ds_read_b128 v[130:133], v150 offset:6144
	ds_read_b128 v[158:161], v150 offset:6656
	ds_read_b64_tr_b16 v[54:55], v162 offset:41984
	ds_read_b64_tr_b16 v[56:57], v162 offset:42496
	v_mfma_f32_32x32x16_bf16 v[82:97], v[134:137], v[102:105], v[82:97]
	v_add_f32_e32 v51, v58, v59
	v_add_f32_e32 v52, v60, v61
	v_add_f32_e32 v51, v51, v52
	v_add_f32_e32 v52, v51, v50
	v_cvt_pk_bf16_f32 v50, v58, v59
	v_cvt_pk_bf16_f32 v51, v60, v61
	ds_read_b64_tr_b16 v[58:59], v162 offset:46080
	ds_read_b64_tr_b16 v[60:61], v162 offset:46592
	v_mfma_f32_32x32x16_bf16 v[66:81], v[126:129], v[102:105], v[66:81]
	v_add_f32_e32 v53, v62, v63
	v_add_f32_e32 v126, v64, v65
	v_add_f32_e32 v53, v53, v126
	v_add_f32_e32 v151, v53, v52
	v_cvt_pk_bf16_f32 v52, v62, v63
	v_cvt_pk_bf16_f32 v53, v64, v65
	ds_read_b128 v[126:129], v150 offset:8192
	ds_read_b128 v[134:137], v150 offset:8704
	ds_read_b64_tr_b16 v[62:63], v162 offset:43008
	ds_read_b64_tr_b16 v[64:65], v162 offset:43520
	v_mfma_f32_32x32x16_bf16 v[82:97], v[122:125], v[106:109], v[82:97]
	v_add_f32_e32 v122, v34, v35
	v_add_f32_e32 v123, v36, v37
	v_add_f32_e32 v122, v122, v123
	v_add_f32_e32 v122, v122, v151
	v_cvt_pk_bf16_f32 v34, v34, v35
	v_cvt_pk_bf16_f32 v35, v36, v37
	ds_read_b64_tr_b16 v[150:151], v162 offset:47104
	ds_read_b64_tr_b16 v[152:153], v162 offset:47616
	v_mfma_f32_32x32x16_bf16 v[66:81], v[118:121], v[106:109], v[66:81]
	v_add_f32_e32 v36, v38, v39
	v_add_f32_e32 v37, v40, v41
	v_add_f32_e32 v36, v36, v37
	v_add_f32_e32 v118, v36, v122
	v_cvt_pk_bf16_f32 v36, v38, v39
	v_cvt_pk_bf16_f32 v37, v40, v41
	ds_read_b64_tr_b16 v[154:155], v162 offset:44032
	ds_read_b64_tr_b16 v[156:157], v162 offset:44544
	s_waitcnt lgkmcnt(13)
	v_mfma_f32_32x32x16_bf16 v[82:97], v[130:133], v[110:113], v[82:97]
	v_add_f32_e32 v38, v42, v43
	v_add_f32_e32 v39, v44, v45
	v_add_f32_e32 v38, v38, v39
	v_add_f32_e32 v40, v38, v118
	v_cvt_pk_bf16_f32 v38, v42, v43
	v_cvt_pk_bf16_f32 v39, v44, v45
	ds_read_b64_tr_b16 v[42:43], v162 offset:48128
	ds_read_b64_tr_b16 v[44:45], v162 offset:48640
	s_waitcnt lgkmcnt(14)
	v_mfma_f32_32x32x16_bf16 v[66:81], v[158:161], v[110:113], v[66:81]
	v_add_f32_e32 v41, v46, v47
	v_add_f32_e32 v118, v48, v49
	v_add_f32_e32 v41, v41, v118
	v_add_f32_e32 v166, v41, v40
	v_cvt_pk_bf16_f32 v40, v46, v47
	v_cvt_pk_bf16_f32 v41, v48, v49
	s_waitcnt lgkmcnt(9)
	v_mfma_f32_32x32x16_bf16 v[82:97], v[126:129], v[114:117], v[82:97]
	s_waitcnt lgkmcnt(8)
	v_mfma_f32_32x32x16_bf16 v[66:81], v[134:137], v[114:117], v[66:81]
	s_add_i32 s61, s44, 2
	s_cmp_lt_i32 s61, s71
	s_cselect_b64 s[52:53], -1, 0
	s_cmp_ge_i32 s61, s71
	s_cselect_b64 s[50:51], -1, 0
	s_and_b64 vcc, exec, s[50:51]
	s_cbranch_vccnz .LBB0_1322
	s_and_b32 s54, s61, 3
	s_mulk_i32 s54, 0x2800
	s_add_i32 s55, s54, s66
	s_mov_b32 m0, s55
	s_nop 0
	global_load_lds_dwordx4 v[222:223], off
	s_and_b64 vcc, exec, s[42:43]
	s_cbranch_vccnz .LBB0_1322
	s_add_i32 s54, s54, s70
	s_mov_b32 m0, s54
	s_nop 0
	global_load_lds_dwordx4 v[220:221], off
.LBB0_1322:
	s_mul_hi_i32 s54, s44, 0x55555556
	s_mul_i32 s54, s54, 3
	s_sub_i32 s54, s44, s54
	s_lshl_b32 s54, s54, 13
	s_add_i32 s54, s54, s72
	s_mov_b32 m0, s54
	s_nop 0
	global_load_lds_dwordx4 v[218:219], off
	s_cmp_lt_i32 s45, s68
	s_cbranch_scc1 .LBB0_1324
	v_add_u32_e32 v47, 0xffffffa5, v195
	v_add_u32_e32 v46, 0xffffff85, v195
	v_cmp_le_i32_e32 vcc, v47, v191
	s_nop 1
	v_cndmask_b32_e32 v66, v230, v66, vcc
	v_cmp_lt_i32_e32 vcc, v46, v191
	s_nop 1
	v_cndmask_b32_e32 v83, v230, v83, vcc
	v_cmp_le_i32_e32 vcc, v46, v191
	v_add_u32_e32 v46, 0xffffffa6, v195
	s_nop 0
	v_cndmask_b32_e32 v82, v230, v82, vcc
	v_cmp_le_i32_e32 vcc, v46, v191
	v_add_u32_e32 v46, 0xffffff87, v195
	s_nop 0
	v_cndmask_b32_e32 v67, v230, v67, vcc
	v_cmp_le_i32_e32 vcc, v46, v191
	v_add_u32_e32 v46, 0xffffffa7, v195
	s_nop 0
	v_cndmask_b32_e32 v84, v230, v84, vcc
	v_cmp_le_i32_e32 vcc, v46, v191
	v_add_u32_e32 v46, 0xffffff88, v195
	s_nop 0
	v_cndmask_b32_e32 v68, v230, v68, vcc
	v_cmp_le_i32_e32 vcc, v46, v191
	v_add_u32_e32 v46, 0xffffffa8, v195
	s_nop 0
	v_cndmask_b32_e32 v85, v230, v85, vcc
	v_cmp_le_i32_e32 vcc, v46, v191
	v_add_u32_e32 v46, 0xffffff8d, v195
	s_nop 0
	v_cndmask_b32_e32 v69, v230, v69, vcc
	v_cmp_le_i32_e32 vcc, v46, v191
	v_add_u32_e32 v46, 0xffffffad, v195
	s_nop 0
	v_cndmask_b32_e32 v86, v230, v86, vcc
	v_cmp_le_i32_e32 vcc, v46, v191
	v_add_u32_e32 v46, 0xffffff8e, v195
	s_nop 0
	v_cndmask_b32_e32 v70, v230, v70, vcc
	v_cmp_le_i32_e32 vcc, v46, v191
	v_add_u32_e32 v46, 0xffffffae, v195
	s_nop 0
	v_cndmask_b32_e32 v87, v230, v87, vcc
	v_cmp_le_i32_e32 vcc, v46, v191
	v_add_u32_e32 v46, 0xffffff8f, v195
	s_nop 0
	v_cndmask_b32_e32 v71, v230, v71, vcc
	v_cmp_le_i32_e32 vcc, v46, v191
	v_add_u32_e32 v46, 0xffffffaf, v195
	s_nop 0
	v_cndmask_b32_e32 v88, v230, v88, vcc
	v_cmp_le_i32_e32 vcc, v46, v191
	v_add_u32_e32 v46, 0xffffff90, v195
	s_nop 0
	v_cndmask_b32_e32 v72, v230, v72, vcc
	v_cmp_le_i32_e32 vcc, v46, v191
	v_add_u32_e32 v46, 0xffffffb0, v195
	s_nop 0
	v_cndmask_b32_e32 v89, v230, v89, vcc
	v_cmp_le_i32_e32 vcc, v46, v191
	v_add_u32_e32 v46, 0xffffff95, v195
	s_nop 0
	v_cndmask_b32_e32 v73, v230, v73, vcc
	v_cmp_le_i32_e32 vcc, v46, v191
	v_add_u32_e32 v46, 0xffffffb5, v195
	s_nop 0
	v_cndmask_b32_e32 v90, v230, v90, vcc
	v_cmp_le_i32_e32 vcc, v46, v191
	v_add_u32_e32 v46, 0xffffff96, v195
	s_nop 0
	v_cndmask_b32_e32 v74, v230, v74, vcc
	v_cmp_le_i32_e32 vcc, v46, v191
	v_add_u32_e32 v46, 0xffffffb6, v195
	s_nop 0
	v_cndmask_b32_e32 v91, v230, v91, vcc
	v_cmp_le_i32_e32 vcc, v46, v191
	v_add_u32_e32 v46, 0xffffff97, v195
	s_nop 0
	v_cndmask_b32_e32 v75, v230, v75, vcc
	v_cmp_le_i32_e32 vcc, v46, v191
	v_add_u32_e32 v46, 0xffffffb7, v195
	s_nop 0
	v_cndmask_b32_e32 v92, v230, v92, vcc
	v_cmp_le_i32_e32 vcc, v46, v191
	v_add_u32_e32 v46, 0xffffff98, v195
	s_nop 0
	v_cndmask_b32_e32 v76, v230, v76, vcc
	v_cmp_le_i32_e32 vcc, v46, v191
	v_add_u32_e32 v46, 0xffffffb8, v195
	s_nop 0
	v_cndmask_b32_e32 v93, v230, v93, vcc
	v_cmp_le_i32_e32 vcc, v46, v191
	v_add_u32_e32 v46, 0xffffff9d, v195
	s_nop 0
	v_cndmask_b32_e32 v77, v230, v77, vcc
	v_cmp_le_i32_e32 vcc, v46, v191
	v_add_u32_e32 v46, 0xffffffbd, v195
	s_nop 0
	v_cndmask_b32_e32 v94, v230, v94, vcc
	v_cmp_le_i32_e32 vcc, v46, v191
	v_add_u32_e32 v46, 0xffffff9e, v195
	s_nop 0
	v_cndmask_b32_e32 v78, v230, v78, vcc
	v_cmp_le_i32_e32 vcc, v46, v191
	v_add_u32_e32 v46, 0xffffffbe, v195
	s_nop 0
	v_cndmask_b32_e32 v95, v230, v95, vcc
	v_cmp_le_i32_e32 vcc, v46, v191
	v_add_u32_e32 v46, 0xffffff9f, v195
	s_nop 0
	v_cndmask_b32_e32 v79, v230, v79, vcc
	v_cmp_le_i32_e32 vcc, v46, v191
	v_add_u32_e32 v46, 0xffffffbf, v195
	s_nop 0
	v_cndmask_b32_e32 v96, v230, v96, vcc
	v_cmp_le_i32_e32 vcc, v46, v191
	v_add_u32_e32 v46, 0xffffffa0, v195
	s_nop 0
	v_cndmask_b32_e32 v80, v230, v80, vcc
	v_cmp_le_i32_e32 vcc, v46, v191
	v_subrev_u32_e32 v46, 64, v195
	s_nop 0
	v_cndmask_b32_e32 v97, v230, v97, vcc
	v_cmp_le_i32_e32 vcc, v46, v191
	s_nop 1
	v_cndmask_b32_e32 v81, v230, v81, vcc
.LBB0_1324:
	v_mfma_f32_32x32x16_bf16 v[2:17], v[138:141], v[142:145], v[2:17]
	v_exp_f32_e32 v82, v82
	v_exp_f32_e32 v83, v83
	v_exp_f32_e32 v84, v84
	v_exp_f32_e32 v85, v85
	v_mfma_f32_32x32x16_bf16 v[18:33], v[138:141], v[146:149], v[18:33]
	v_exp_f32_e32 v86, v86
	v_exp_f32_e32 v87, v87
	v_exp_f32_e32 v88, v88
	v_exp_f32_e32 v89, v89
	s_and_b32 s54, s44, 3
	s_mulk_i32 s54, 0x2800
	v_add_u32_e32 v197, s54, v238
	ds_read_b128 v[138:141], v197
	ds_read_b128 v[130:133], v197 offset:512
	v_mfma_f32_32x32x16_bf16 v[2:17], v[50:53], v[54:57], v[2:17]
	v_exp_f32_e32 v90, v90
	v_exp_f32_e32 v91, v91
	v_exp_f32_e32 v92, v92
	v_exp_f32_e32 v93, v93
	ds_read_b128 v[134:137], v197 offset:2048
	ds_read_b128 v[126:129], v197 offset:2560
	v_mfma_f32_32x32x16_bf16 v[18:33], v[50:53], v[58:61], v[18:33]
	v_exp_f32_e32 v94, v94
	v_exp_f32_e32 v95, v95
	v_exp_f32_e32 v96, v96
	v_exp_f32_e32 v97, v97
	ds_read_b128 v[122:125], v197 offset:4096
	ds_read_b128 v[118:121], v197 offset:4608
	s_waitcnt lgkmcnt(12)
	v_mfma_f32_32x32x16_bf16 v[2:17], v[34:37], v[62:65], v[2:17]
	v_exp_f32_e32 v66, v66
	v_exp_f32_e32 v67, v67
	v_exp_f32_e32 v68, v68
	v_exp_f32_e32 v69, v69
	s_waitcnt lgkmcnt(10)
	v_mfma_f32_32x32x16_bf16 v[18:33], v[34:37], v[150:153], v[18:33]
	v_exp_f32_e32 v70, v70
	v_exp_f32_e32 v71, v71
	v_exp_f32_e32 v72, v72
	v_exp_f32_e32 v73, v73
	s_waitcnt lgkmcnt(8)
	v_mfma_f32_32x32x16_bf16 v[2:17], v[38:41], v[154:157], v[2:17]
	v_exp_f32_e32 v74, v74
	v_exp_f32_e32 v75, v75
	v_exp_f32_e32 v76, v76
	v_exp_f32_e32 v77, v77
	s_waitcnt lgkmcnt(6)
	v_mfma_f32_32x32x16_bf16 v[18:33], v[38:41], v[42:45], v[18:33]
	v_exp_f32_e32 v78, v78
	v_exp_f32_e32 v79, v79
	v_exp_f32_e32 v80, v80
	v_exp_f32_e32 v81, v81
	s_and_b64 s[52:53], s[52:53], exec
	s_cselect_b32 s54, s60, 1
	s_cmp_gt_i32 s54, 2
	s_mov_b64 s[52:53], -1
	s_cbranch_scc0 .LBB0_1326
	s_waitcnt vmcnt(3) lgkmcnt(0)
	s_barrier
	s_mov_b64 s[52:53], 0

.LBB0_1331:
	s_mul_hi_i32 s52, s45, 0x55555556
	s_mul_i32 s52, s52, 3
	s_sub_i32 s45, s45, s52
	v_lshl_add_u32 v199, s45, 13, v240
	ds_read_b64_tr_b16 v[162:163], v199 offset:40960
	ds_read_b64_tr_b16 v[164:165], v199 offset:41472
	s_waitcnt lgkmcnt(7)
	v_mfma_f32_32x32x16_bf16 v[50:65], v[138:141], v[98:101], 0
	v_add_f32_e32 v34, v82, v83
	v_add_f32_e32 v35, v84, v85
	v_add_f32_e32 v34, v34, v35
	v_add_f32_e32 v34, 0, v34
	v_cvt_pk_bf16_f32 v154, v82, v83
	v_cvt_pk_bf16_f32 v155, v84, v85
	ds_read_b64_tr_b16 v[158:159], v199 offset:45056
	ds_read_b64_tr_b16 v[160:161], v199 offset:45568
	v_add_f32_e32 v35, v86, v87
	v_add_f32_e32 v36, v88, v89
	v_add_f32_e32 v35, v35, v36
	v_add_f32_e32 v82, v35, v34
	s_waitcnt lgkmcnt(8)
	v_mfma_f32_32x32x16_bf16 v[34:49], v[130:133], v[98:101], 0
	v_cvt_pk_bf16_f32 v156, v86, v87
	v_cvt_pk_bf16_f32 v157, v88, v89
	ds_read_b128 v[170:173], v197 offset:6144
	ds_read_b128 v[174:177], v197 offset:6656
	ds_read_b64_tr_b16 v[150:151], v199 offset:41984
	ds_read_b64_tr_b16 v[152:153], v199 offset:42496
	s_waitcnt lgkmcnt(11)
	v_mfma_f32_32x32x16_bf16 v[50:65], v[134:137], v[102:105], v[50:65]
	v_add_f32_e32 v83, v90, v91
	v_add_f32_e32 v84, v92, v93
	v_add_f32_e32 v83, v83, v84
	v_add_f32_e32 v82, v83, v82
	v_cvt_pk_bf16_f32 v142, v90, v91
	v_cvt_pk_bf16_f32 v143, v92, v93
	ds_read_b64_tr_b16 v[146:147], v199 offset:46080
	ds_read_b64_tr_b16 v[148:149], v199 offset:46592
	s_waitcnt lgkmcnt(12)
	v_mfma_f32_32x32x16_bf16 v[34:49], v[126:129], v[102:105], v[34:49]
	v_add_f32_e32 v83, v94, v95
	v_add_f32_e32 v84, v96, v97
	v_add_f32_e32 v83, v83, v84
	v_add_f32_e32 v82, v83, v82
	v_cvt_pk_bf16_f32 v144, v94, v95
	v_cvt_pk_bf16_f32 v145, v96, v97
	ds_read_b128 v[248:251], v197 offset:8192
	ds_read_b128 v[232:235], v197 offset:8704
	ds_read_b64_tr_b16 v[90:91], v199 offset:43008
	ds_read_b64_tr_b16 v[92:93], v199 offset:43520
	s_waitcnt lgkmcnt(14)
	v_mfma_f32_32x32x16_bf16 v[50:65], v[122:125], v[106:109], v[50:65]
	v_add_f32_e32 v83, v66, v67
	v_add_f32_e32 v84, v68, v69
	v_add_f32_e32 v83, v83, v84
	v_add_f32_e32 v84, v83, v82
	v_cvt_pk_bf16_f32 v82, v66, v67
	v_cvt_pk_bf16_f32 v83, v68, v69
	ds_read_b64_tr_b16 v[86:87], v199 offset:47104
	ds_read_b64_tr_b16 v[88:89], v199 offset:47616
	v_mfma_f32_32x32x16_bf16 v[34:49], v[118:121], v[106:109], v[34:49]
	v_add_f32_e32 v66, v70, v71
	v_add_f32_e32 v67, v72, v73
	v_add_f32_e32 v66, v66, v67
	v_add_f32_e32 v66, v66, v84
	v_cvt_pk_bf16_f32 v84, v70, v71
	v_cvt_pk_bf16_f32 v85, v72, v73
	ds_read_b64_tr_b16 v[70:71], v199 offset:44032
	ds_read_b64_tr_b16 v[72:73], v199 offset:44544
	s_waitcnt lgkmcnt(13)
	v_mfma_f32_32x32x16_bf16 v[50:65], v[170:173], v[110:113], v[50:65]
	v_add_f32_e32 v67, v74, v75
	v_add_f32_e32 v68, v76, v77
	v_add_f32_e32 v67, v67, v68
	v_add_f32_e32 v68, v67, v66
	v_cvt_pk_bf16_f32 v66, v74, v75
	v_cvt_pk_bf16_f32 v67, v76, v77
	ds_read_b64_tr_b16 v[74:75], v199 offset:48128
	ds_read_b64_tr_b16 v[76:77], v199 offset:48640
	s_waitcnt lgkmcnt(14)
	v_mfma_f32_32x32x16_bf16 v[34:49], v[174:177], v[110:113], v[34:49]
	v_add_f32_e32 v69, v78, v79
	v_add_f32_e32 v94, v80, v81
	v_add_f32_e32 v69, v69, v94
	v_add_f32_e32 v94, v69, v68
	v_cvt_pk_bf16_f32 v68, v78, v79
	v_cvt_pk_bf16_f32 v69, v80, v81
	s_waitcnt lgkmcnt(9)
	v_mfma_f32_32x32x16_bf16 v[50:65], v[248:251], v[114:117], v[50:65]
	s_waitcnt lgkmcnt(8)
	v_mfma_f32_32x32x16_bf16 v[34:49], v[232:235], v[114:117], v[34:49]
	s_add_i32 s54, s44, 3
	s_cmp_lt_i32 s54, s71
	s_cselect_b64 s[52:53], -1, 0
	s_cmp_ge_i32 s54, s71
	s_cbranch_scc1 .LBB0_1334
	s_ashr_i32 s55, s54, 31
	s_and_b32 s45, s54, 3
	s_lshl_b64 s[58:59], s[54:55], 17
	s_mulk_i32 s45, 0x2800
	v_lshl_add_u64 v[78:79], v[212:213], 0, s[58:59]
	s_add_i32 s58, s45, s66
	s_mov_b32 m0, s58
	s_nop 0
	global_load_lds_dwordx4 v[78:79], off
	s_and_b64 vcc, exec, s[42:43]
	s_cbranch_vccnz .LBB0_1334
	s_lshl_b64 s[54:55], s[54:55], 11
	s_add_i32 s45, s45, s70
	v_lshl_add_u64 v[78:79], v[214:215], 0, s[54:55]
	s_mov_b32 m0, s45
	s_nop 0
	global_load_lds_dwordx4 v[78:79], off
.LBB0_1334:
	s_add_i32 s54, s44, 1
	s_cmp_lt_i32 s54, s71
	s_cselect_b64 s[58:59], -1, 0
	s_cmp_ge_i32 s54, s71
	s_cbranch_scc1 .LBB0_1336
	s_mul_hi_i32 s45, s54, 0x55555556
	s_mul_i32 s45, s45, 3
	s_sub_i32 s45, s54, s45
	s_ashr_i32 s55, s54, 31
	s_lshl_b64 s[62:63], s[54:55], 17
	s_lshl_b32 s45, s45, 13
	v_lshl_add_u64 v[78:79], v[216:217], 0, s[62:63]
	s_add_i32 s45, s45, s72
	s_mov_b32 m0, s45
	s_nop 0
	global_load_lds_dwordx4 v[78:79], off

.LBB0_1338:
	v_mfma_f32_32x32x16_bf16 v[2:17], v[154:157], v[162:165], v[2:17]
	v_exp_f32_e32 v50, v50
	v_exp_f32_e32 v51, v51
	v_exp_f32_e32 v52, v52
	v_exp_f32_e32 v53, v53
	v_mfma_f32_32x32x16_bf16 v[18:33], v[154:157], v[158:161], v[18:33]
	v_exp_f32_e32 v54, v54
	v_exp_f32_e32 v55, v55
	v_exp_f32_e32 v56, v56
	v_exp_f32_e32 v57, v57
	v_cndmask_b32_e64 v78, 0, 1, s[58:59]
	v_cmp_ne_u32_e64 s[44:45], 1, v78
	s_andn2_b64 vcc, exec, s[58:59]
	s_cbranch_vccnz .LBB0_1340
	s_and_b32 s55, s54, 3
	s_mulk_i32 s55, 0x2800
	v_add_u32_e32 v79, s55, v238
	ds_read_b128 v[138:141], v79
	ds_read_b128 v[130:133], v79 offset:512
.LBB0_1340:
	v_mfma_f32_32x32x16_bf16 v[2:17], v[142:145], v[150:153], v[2:17]
	v_exp_f32_e32 v58, v58
	v_exp_f32_e32 v59, v59
	v_exp_f32_e32 v60, v60
	v_exp_f32_e32 v61, v61
	s_and_b64 vcc, exec, s[44:45]
	s_cbranch_vccnz .LBB0_1342
	s_and_b32 s55, s54, 3
	s_mulk_i32 s55, 0x2800
	v_add_u32_e32 v79, s55, v238
	ds_read_b128 v[134:137], v79 offset:2048
	ds_read_b128 v[126:129], v79 offset:2560
.LBB0_1342:
	v_mfma_f32_32x32x16_bf16 v[18:33], v[142:145], v[146:149], v[18:33]
	v_exp_f32_e32 v62, v62
	v_exp_f32_e32 v63, v63
	v_exp_f32_e32 v64, v64
	v_exp_f32_e32 v65, v65
	s_and_b64 vcc, exec, s[44:45]
	s_cbranch_vccnz .LBB0_1344
	s_and_b32 s44, s54, 3
	s_mulk_i32 s44, 0x2800
	v_add_u32_e32 v79, s44, v238
	ds_read_b128 v[122:125], v79 offset:4096
	ds_read_b128 v[118:121], v79 offset:4608

.LBB0_1360:
	s_mov_b32 m0, s100
	s_add_i32 s71, s71, -1
	s_mul_hi_u32 s42, s71, 0xaaaaaaab
	s_lshr_b32 s42, s42, 1
	s_mul_i32 s42, s42, 3
	s_sub_i32 s42, s71, s42
	v_lshl_add_u32 v66, s42, 13, v240
	ds_read_b64_tr_b16 v[68:69], v66 offset:40960
	ds_read_b64_tr_b16 v[70:71], v66 offset:41472
	ds_read_b64_tr_b16 v[72:73], v66 offset:41984
	ds_read_b64_tr_b16 v[74:75], v66 offset:42496
	ds_read_b64_tr_b16 v[76:77], v66 offset:43008
	ds_read_b64_tr_b16 v[78:79], v66 offset:43520
	ds_read_b64_tr_b16 v[80:81], v66 offset:44032
	ds_read_b64_tr_b16 v[82:83], v66 offset:44544
	ds_read_b64_tr_b16 v[84:85], v66 offset:45056
	ds_read_b64_tr_b16 v[86:87], v66 offset:45568
	ds_read_b64_tr_b16 v[88:89], v66 offset:46080
	ds_read_b64_tr_b16 v[90:91], v66 offset:46592
	ds_read_b64_tr_b16 v[92:93], v66 offset:47104
	ds_read_b64_tr_b16 v[94:95], v66 offset:47616
	ds_read_b64_tr_b16 v[96:97], v66 offset:48128
	ds_read_b64_tr_b16 v[98:99], v66 offset:48640
	v_add_f32_e32 v66, v50, v51
	v_add_f32_e32 v67, v52, v53
	v_add_f32_e32 v66, v66, v67
	v_add_f32_e32 v66, 0, v66
	v_add_f32_e32 v67, v54, v55
	v_add_f32_e32 v100, v56, v57
	v_add_f32_e32 v67, v67, v100
	v_add_f32_e32 v66, v67, v66
	v_add_f32_e32 v67, v58, v59
	v_add_f32_e32 v100, v60, v61
	v_add_f32_e32 v67, v67, v100
	v_add_f32_e32 v66, v67, v66
	v_add_f32_e32 v67, v62, v63
	v_add_f32_e32 v100, v64, v65
	v_add_f32_e32 v67, v67, v100
	v_add_f32_e32 v66, v67, v66
	v_add_f32_e32 v67, v34, v35
	v_add_f32_e32 v100, v36, v37
	v_add_f32_e32 v67, v67, v100
	v_add_f32_e32 v66, v67, v66
	v_add_f32_e32 v67, v38, v39
	v_add_f32_e32 v100, v40, v41
	v_add_f32_e32 v67, v67, v100
	v_add_f32_e32 v66, v67, v66
	v_add_f32_e32 v67, v42, v43
	v_add_f32_e32 v100, v44, v45
	v_add_f32_e32 v67, v67, v100
	v_add_f32_e32 v66, v67, v66
	v_add_f32_e32 v67, v46, v47
	v_add_f32_e32 v100, v48, v49
	v_add_f32_e32 v67, v67, v100
	s_mov_b64 s[72:73], 0xe800000
	v_add_f32_e32 v66, v67, v66
	v_cvt_pk_bf16_f32 v50, v50, v51
	v_cvt_pk_bf16_f32 v51, v52, v53
	v_cvt_pk_bf16_f32 v52, v54, v55
	v_cvt_pk_bf16_f32 v53, v56, v57
	v_cvt_pk_bf16_f32 v54, v58, v59
	v_cvt_pk_bf16_f32 v55, v60, v61
	v_cvt_pk_bf16_f32 v56, v62, v63
	v_cvt_pk_bf16_f32 v57, v64, v65
	v_cvt_pk_bf16_f32 v34, v34, v35
	v_cvt_pk_bf16_f32 v35, v36, v37
	v_cvt_pk_bf16_f32 v36, v38, v39
	v_cvt_pk_bf16_f32 v37, v40, v41
	v_cvt_pk_bf16_f32 v38, v42, v43
	v_cvt_pk_bf16_f32 v39, v44, v45
	v_cvt_pk_bf16_f32 v40, v46, v47
	v_cvt_pk_bf16_f32 v41, v48, v49
	s_waitcnt lgkmcnt(14)
	v_mfma_f32_32x32x16_bf16 v[2:17], v[50:53], v[68:71], v[2:17]
	s_waitcnt lgkmcnt(6)
	v_mfma_f32_32x32x16_bf16 v[18:33], v[50:53], v[84:87], v[18:33]
	v_mfma_f32_32x32x16_bf16 v[2:17], v[54:57], v[72:75], v[2:17]
	s_waitcnt lgkmcnt(4)
	v_mfma_f32_32x32x16_bf16 v[18:33], v[54:57], v[88:91], v[18:33]
	v_mfma_f32_32x32x16_bf16 v[2:17], v[34:37], v[76:79], v[2:17]
	s_waitcnt lgkmcnt(2)
	v_mfma_f32_32x32x16_bf16 v[18:33], v[34:37], v[92:95], v[18:33]
	v_mfma_f32_32x32x16_bf16 v[2:17], v[38:41], v[80:83], v[2:17]
	s_waitcnt lgkmcnt(0)
	v_mfma_f32_32x32x16_bf16 v[18:33], v[38:41], v[96:99], v[18:33]
	v_mov_b32_e32 v50, 0
	s_and_saveexec_b64 s[42:43], s[38:39]
	s_mov_b64 s[70:71], 0xe800800
	s_cbranch_execz .LBB0_1364
	s_mov_b64 s[50:51], exec
	v_mbcnt_lo_u32_b32 v34, s50, 0
	v_mbcnt_hi_u32_b32 v34, s51, v34
	v_cmp_eq_u32_e32 vcc, 0, v34
	s_and_saveexec_b64 s[44:45], vcc
	s_cbranch_execz .LBB0_1363
	s_bcnt1_i32_b64 s50, s[50:51]
	v_mov_b32_e32 v35, s50
	global_atomic_add v35, v167, v35, s[36:37] sc0

.LBB0_1441:
	v_lshl_add_u32 v140, s50, 8, v146
	v_lshl_or_b32 v142, s51, 8, v148
	v_ashrrev_i32_e32 v141, 31, v140
	v_lshlrev_b64 v[140:141], 11, v[140:141]
	v_ashrrev_i32_e32 v143, 31, v142
	v_lshl_add_u64 v[140:141], s[26:27], 0, v[140:141]
	v_lshl_add_u64 v[140:141], v[142:143], 1, v[140:141]
	global_load_dwordx4 v[142:145] v[140:141], off
	global_load_dwordx4 v[150:153] v[140:141], off offset:256
	s_mov_b32 s41, 0x8000
	s_mov_b64 s[50:51], 0x18000
	s_waitcnt vmcnt(0) lgkmcnt(0)
	v_lshlrev_b32_e32 v162, 16, v144
	v_and_b32_e32 v163, 0xffff0000, v144
	v_add_co_u32_e32 v144, vcc, s41, v140
	v_lshlrev_b32_e32 v158, 16, v142
	v_and_b32_e32 v159, 0xffff0000, v142
	v_lshlrev_b32_e32 v160, 16, v143
	v_and_b32_e32 v161, 0xffff0000, v143
	v_lshlrev_b32_e32 v164, 16, v145
	v_and_b32_e32 v165, 0xffff0000, v145
	v_addc_co_u32_e32 v145, vcc, 0, v141, vcc
	v_lshlrev_b32_e32 v170, 16, v150
	v_and_b32_e32 v171, 0xffff0000, v150
	v_lshlrev_b32_e32 v172, 16, v151
	v_and_b32_e32 v173, 0xffff0000, v151
	v_lshlrev_b32_e32 v174, 16, v152
	v_and_b32_e32 v175, 0xffff0000, v152
	v_lshlrev_b32_e32 v176, 16, v153
	v_and_b32_e32 v177, 0xffff0000, v153
	v_lshl_add_u64 v[142:143], v[140:141], 0, s[4:5]
	global_load_dwordx4 v[150:153] v[144:145], off
	global_load_dwordx4 v[154:157] v[142:143], off offset:256
	v_pk_add_f32 v[128:129], v[128:129], v[160:161]
	v_pk_add_f32 v[126:127], v[126:127], v[158:159]
	v_pk_add_f32 v[158:159], v[124:125], v[164:165]
	v_pk_add_f32 v[124:125], v[122:123], v[162:163]
	v_cvt_pk_bf16_f32 v122, v126, v127
	v_cvt_pk_bf16_f32 v123, v128, v129
	v_pk_add_f32 v[120:121], v[120:121], v[172:173]
	v_cvt_pk_bf16_f32 v124, v124, v125
	v_cvt_pk_bf16_f32 v125, v158, v159
	global_store_dwordx4 v[140:141], v[122:125], off
	v_pk_add_f32 v[118:119], v[118:119], v[170:171]
	s_mov_b32 s41, 0x10000
	v_pk_add_f32 v[122:123], v[116:117], v[176:177]
	v_pk_add_f32 v[116:117], v[114:115], v[174:175]
	v_cvt_pk_bf16_f32 v114, v118, v119
	v_cvt_pk_bf16_f32 v115, v120, v121
	s_waitcnt vmcnt(1) lgkmcnt(0)
	v_lshlrev_b32_e32 v126, 16, v150
	v_cvt_pk_bf16_f32 v116, v116, v117
	v_cvt_pk_bf16_f32 v117, v122, v123
	global_store_dwordx4 v[140:141], v[114:117], off offset:256
	v_and_b32_e32 v127, 0xffff0000, v150
	v_lshlrev_b32_e32 v128, 16, v151
	v_add_co_u32_e32 v116, vcc, s41, v140
	v_lshl_add_u64 v[114:115], v[140:141], 0, s[6:7]
	s_nop 0
	v_addc_co_u32_e32 v117, vcc, 0, v141, vcc
	global_load_dwordx4 v[118:121] v[116:117], off
	global_load_dwordx4 v[122:125] v[114:115], off offset:256
	v_and_b32_e32 v129, 0xffff0000, v151
	v_lshlrev_b32_e32 v150, 16, v152
	v_and_b32_e32 v151, 0xffff0000, v152
	v_lshlrev_b32_e32 v152, 16, v153
	v_and_b32_e32 v153, 0xffff0000, v153
	v_lshlrev_b32_e32 v160, 16, v156
	v_and_b32_e32 v161, 0xffff0000, v156
	v_lshlrev_b32_e32 v156, 16, v157
	v_and_b32_e32 v157, 0xffff0000, v157
	v_pk_add_f32 v[112:113], v[112:113], v[128:129]
	v_pk_add_f32 v[110:111], v[110:111], v[126:127]
	v_pk_add_f32 v[126:127], v[108:109], v[152:153]
	v_pk_add_f32 v[108:109], v[106:107], v[150:151]
	v_cvt_pk_bf16_f32 v106, v110, v111
	v_cvt_pk_bf16_f32 v107, v112, v113
	v_lshlrev_b32_e32 v158, 16, v154
	v_and_b32_e32 v159, 0xffff0000, v154
	v_lshlrev_b32_e32 v154, 16, v155
	v_and_b32_e32 v155, 0xffff0000, v155
	v_cvt_pk_bf16_f32 v108, v108, v109
	v_cvt_pk_bf16_f32 v109, v126, v127
	global_store_dwordx4 v[144:145], v[106:109], off
	v_pk_add_f32 v[104:105], v[104:105], v[154:155]
	v_pk_add_f32 v[102:103], v[102:103], v[158:159]
	v_pk_add_f32 v[106:107], v[100:101], v[156:157]
	v_pk_add_f32 v[100:101], v[98:99], v[160:161]
	v_cvt_pk_bf16_f32 v98, v102, v103
	v_cvt_pk_bf16_f32 v99, v104, v105
	s_mov_b32 s41, 0x18000
	v_cvt_pk_bf16_f32 v100, v100, v101
	v_cvt_pk_bf16_f32 v101, v106, v107
	global_store_dwordx4 v[142:143], v[98:101], off offset:256
	s_waitcnt vmcnt(2) lgkmcnt(0)
	v_lshlrev_b32_e32 v104, 16, v118
	v_add_co_u32_e32 v100, vcc, s41, v140
	v_and_b32_e32 v105, 0xffff0000, v118
	v_lshlrev_b32_e32 v112, 16, v119
	v_and_b32_e32 v113, 0xffff0000, v119
	v_lshlrev_b32_e32 v110, 16, v120
	v_and_b32_e32 v111, 0xffff0000, v120
	v_lshlrev_b32_e32 v120, 16, v121
	v_and_b32_e32 v121, 0xffff0000, v121
	v_addc_co_u32_e32 v101, vcc, 0, v141, vcc
	v_lshlrev_b32_e32 v102, 16, v122
	v_and_b32_e32 v103, 0xffff0000, v122
	v_lshlrev_b32_e32 v108, 16, v123
	v_and_b32_e32 v109, 0xffff0000, v123
	v_lshlrev_b32_e32 v106, 16, v124
	v_and_b32_e32 v107, 0xffff0000, v124
	v_lshlrev_b32_e32 v118, 16, v125
	v_and_b32_e32 v119, 0xffff0000, v125
	v_lshl_add_u64 v[98:99], v[140:141], 0, s[50:51]
	global_load_dwordx4 v[122:125] v[100:101], off
	global_load_dwordx4 v[126:129] v[98:99], off offset:256
	v_pk_add_f32 v[96:97], v[96:97], v[112:113]
	v_pk_add_f32 v[94:95], v[94:95], v[104:105]
	v_pk_add_f32 v[104:105], v[92:93], v[120:121]
	v_pk_add_f32 v[92:93], v[90:91], v[110:111]
	v_cvt_pk_bf16_f32 v90, v94, v95
	v_cvt_pk_bf16_f32 v91, v96, v97
	v_pk_add_f32 v[88:89], v[88:89], v[108:109]
	v_cvt_pk_bf16_f32 v92, v92, v93
	v_cvt_pk_bf16_f32 v93, v104, v105
	global_store_dwordx4 v[116:117], v[90:93], off
	v_pk_add_f32 v[86:87], v[86:87], v[102:103]
	s_mov_b32 s41, 0x40000
	v_pk_add_f32 v[90:91], v[84:85], v[118:119]
	v_pk_add_f32 v[84:85], v[82:83], v[106:107]
	v_cvt_pk_bf16_f32 v82, v86, v87
	v_cvt_pk_bf16_f32 v83, v88, v89
	s_mov_b64 s[50:51], 0x48000
	v_cvt_pk_bf16_f32 v84, v84, v85
	v_cvt_pk_bf16_f32 v85, v90, v91
	global_store_dwordx4 v[114:115], v[82:85], off offset:256
	s_waitcnt vmcnt(2) lgkmcnt(0)
	v_lshlrev_b32_e32 v94, 16, v122
	v_add_co_u32_e32 v84, vcc, s41, v140
	v_lshl_add_u64 v[82:83], v[140:141], 0, s[82:83]
	s_nop 0
	v_addc_co_u32_e32 v85, vcc, 0, v141, vcc
	global_load_dwordx4 v[86:89] v[84:85], off
	global_load_dwordx4 v[90:93] v[82:83], off offset:256
	v_and_b32_e32 v95, 0xffff0000, v122
	v_lshlrev_b32_e32 v96, 16, v123
	v_and_b32_e32 v97, 0xffff0000, v123
	v_lshlrev_b32_e32 v102, 16, v124
	v_and_b32_e32 v103, 0xffff0000, v124
	v_lshlrev_b32_e32 v104, 16, v125
	v_and_b32_e32 v105, 0xffff0000, v125
	v_lshlrev_b32_e32 v110, 16, v128
	v_and_b32_e32 v111, 0xffff0000, v128
	v_lshlrev_b32_e32 v112, 16, v129
	v_and_b32_e32 v113, 0xffff0000, v129
	v_pk_add_f32 v[80:81], v[80:81], v[96:97]
	v_pk_add_f32 v[78:79], v[78:79], v[94:95]
	v_pk_add_f32 v[94:95], v[76:77], v[104:105]
	v_pk_add_f32 v[76:77], v[74:75], v[102:103]
	v_cvt_pk_bf16_f32 v74, v78, v79
	v_cvt_pk_bf16_f32 v75, v80, v81
	v_lshlrev_b32_e32 v106, 16, v126
	v_and_b32_e32 v107, 0xffff0000, v126
	v_lshlrev_b32_e32 v108, 16, v127
	v_and_b32_e32 v109, 0xffff0000, v127
	v_cvt_pk_bf16_f32 v76, v76, v77
	v_cvt_pk_bf16_f32 v77, v94, v95
	global_store_dwordx4 v[100:101], v[74:77], off
	v_pk_add_f32 v[72:73], v[72:73], v[108:109]
	v_pk_add_f32 v[70:71], v[70:71], v[106:107]
	v_pk_add_f32 v[74:75], v[68:69], v[112:113]
	v_pk_add_f32 v[68:69], v[66:67], v[110:111]
	v_cvt_pk_bf16_f32 v66, v70, v71
	v_cvt_pk_bf16_f32 v67, v72, v73
	s_mov_b32 s41, 0x48000
	v_cvt_pk_bf16_f32 v68, v68, v69
	v_cvt_pk_bf16_f32 v69, v74, v75
	global_store_dwordx4 v[98:99], v[66:69], off offset:256
	s_waitcnt vmcnt(2) lgkmcnt(0)
	v_lshlrev_b32_e32 v72, 16, v86
	v_add_co_u32_e32 v68, vcc, s41, v140
	v_and_b32_e32 v73, 0xffff0000, v86
	v_lshlrev_b32_e32 v80, 16, v87
	v_and_b32_e32 v81, 0xffff0000, v87
	v_lshlrev_b32_e32 v78, 16, v88
	v_and_b32_e32 v79, 0xffff0000, v88
	v_lshlrev_b32_e32 v88, 16, v89
	v_and_b32_e32 v89, 0xffff0000, v89
	v_addc_co_u32_e32 v69, vcc, 0, v141, vcc
	v_lshlrev_b32_e32 v70, 16, v90
	v_and_b32_e32 v71, 0xffff0000, v90
	v_lshlrev_b32_e32 v76, 16, v91
	v_and_b32_e32 v77, 0xffff0000, v91
	v_lshlrev_b32_e32 v74, 16, v92
	v_and_b32_e32 v75, 0xffff0000, v92
	v_lshlrev_b32_e32 v86, 16, v93
	v_and_b32_e32 v87, 0xffff0000, v93
	v_lshl_add_u64 v[66:67], v[140:141], 0, s[50:51]
	global_load_dwordx4 v[90:93] v[68:69], off
	global_load_dwordx4 v[94:97] v[66:67], off offset:256
	v_pk_add_f32 v[64:65], v[64:65], v[80:81]
	v_pk_add_f32 v[62:63], v[62:63], v[72:73]
	v_pk_add_f32 v[72:73], v[60:61], v[88:89]
	v_pk_add_f32 v[60:61], v[58:59], v[78:79]
	v_cvt_pk_bf16_f32 v58, v62, v63
	v_cvt_pk_bf16_f32 v59, v64, v65
	v_pk_add_f32 v[56:57], v[56:57], v[76:77]
	v_cvt_pk_bf16_f32 v60, v60, v61
	v_cvt_pk_bf16_f32 v61, v72, v73
	global_store_dwordx4 v[84:85], v[58:61], off
	v_pk_add_f32 v[54:55], v[54:55], v[70:71]
	s_mov_b32 s41, 0x50000
	v_pk_add_f32 v[58:59], v[52:53], v[86:87]
	v_pk_add_f32 v[52:53], v[50:51], v[74:75]
	v_cvt_pk_bf16_f32 v50, v54, v55
	v_cvt_pk_bf16_f32 v51, v56, v57
	s_mov_b64 s[50:51], 0x50000
	v_cvt_pk_bf16_f32 v52, v52, v53
	v_cvt_pk_bf16_f32 v53, v58, v59
	global_store_dwordx4 v[82:83], v[50:53], off offset:256
	s_waitcnt vmcnt(2) lgkmcnt(0)
	v_lshlrev_b32_e32 v54, 16, v90
	v_add_co_u32_e32 v52, vcc, s41, v140
	v_lshl_add_u64 v[50:51], v[140:141], 0, s[50:51]
	s_nop 0
	v_addc_co_u32_e32 v53, vcc, 0, v141, vcc
	global_load_dwordx4 v[58:61] v[52:53], off
	global_load_dwordx4 v[62:65] v[50:51], off offset:256
	v_and_b32_e32 v55, 0xffff0000, v90
	v_lshlrev_b32_e32 v56, 16, v91
	v_and_b32_e32 v57, 0xffff0000, v91
	v_lshlrev_b32_e32 v70, 16, v92
	v_and_b32_e32 v71, 0xffff0000, v92
	v_lshlrev_b32_e32 v72, 16, v93
	v_and_b32_e32 v73, 0xffff0000, v93
	v_lshlrev_b32_e32 v78, 16, v96
	v_and_b32_e32 v79, 0xffff0000, v96
	v_lshlrev_b32_e32 v80, 16, v97
	v_and_b32_e32 v81, 0xffff0000, v97
	v_pk_add_f32 v[48:49], v[48:49], v[56:57]
	v_pk_add_f32 v[46:47], v[46:47], v[54:55]
	v_pk_add_f32 v[54:55], v[44:45], v[72:73]
	v_pk_add_f32 v[44:45], v[42:43], v[70:71]
	v_cvt_pk_bf16_f32 v42, v46, v47
	v_cvt_pk_bf16_f32 v43, v48, v49
	v_lshlrev_b32_e32 v74, 16, v94
	v_and_b32_e32 v75, 0xffff0000, v94
	v_lshlrev_b32_e32 v76, 16, v95
	v_and_b32_e32 v77, 0xffff0000, v95
	v_cvt_pk_bf16_f32 v44, v44, v45
	v_cvt_pk_bf16_f32 v45, v54, v55
	global_store_dwordx4 v[68:69], v[42:45], off
	s_mov_b32 s41, 0x58000
	v_pk_add_f32 v[40:41], v[40:41], v[76:77]
	v_pk_add_f32 v[42:43], v[36:37], v[80:81]
	v_pk_add_f32 v[36:37], v[34:35], v[78:79]
	v_pk_add_f32 v[38:39], v[38:39], v[74:75]
	s_mov_b64 s[50:51], 0x58000
	v_cvt_pk_bf16_f32 v34, v38, v39
	v_cvt_pk_bf16_f32 v35, v40, v41
	v_cvt_pk_bf16_f32 v36, v36, v37
	v_cvt_pk_bf16_f32 v37, v42, v43
	global_store_dwordx4 v[66:67], v[34:37], off offset:256
	v_lshl_add_u64 v[46:47], v[140:141], 0, s[50:51]
	s_mov_b64 s[50:51], -1
	s_waitcnt vmcnt(2) lgkmcnt(0)
	v_lshlrev_b32_e32 v48, 16, v60
	v_and_b32_e32 v49, 0xffff0000, v60
	v_add_co_u32_e32 v60, vcc, s41, v140
	v_lshlrev_b32_e32 v54, 16, v61
	v_and_b32_e32 v55, 0xffff0000, v61
	v_addc_co_u32_e32 v61, vcc, 0, v141, vcc
	v_lshlrev_b32_e32 v42, 16, v62
	v_and_b32_e32 v43, 0xffff0000, v62
	v_lshlrev_b32_e32 v44, 16, v63
	v_and_b32_e32 v45, 0xffff0000, v63
	v_lshlrev_b32_e32 v38, 16, v64
	v_and_b32_e32 v39, 0xffff0000, v64
	v_lshlrev_b32_e32 v40, 16, v65
	v_and_b32_e32 v41, 0xffff0000, v65
	global_load_dwordx4 v[34:37] v[60:61], off
	global_load_dwordx4 v[62:65] v[46:47], off offset:256
	v_lshlrev_b32_e32 v56, 16, v58
	v_and_b32_e32 v57, 0xffff0000, v58
	v_lshlrev_b32_e32 v58, 16, v59
	v_and_b32_e32 v59, 0xffff0000, v59
	v_pk_add_f32 v[32:33], v[32:33], v[58:59]
	v_pk_add_f32 v[30:31], v[30:31], v[56:57]
	v_pk_add_f32 v[54:55], v[28:29], v[54:55]
	v_pk_add_f32 v[28:29], v[26:27], v[48:49]
	v_cvt_pk_bf16_f32 v26, v30, v31
	v_cvt_pk_bf16_f32 v27, v32, v33
	v_pk_add_f32 v[24:25], v[24:25], v[44:45]
	v_cvt_pk_bf16_f32 v28, v28, v29
	v_cvt_pk_bf16_f32 v29, v54, v55
	global_store_dwordx4 v[52:53], v[26:29], off
	v_pk_add_f32 v[22:23], v[22:23], v[42:43]
	s_andn2_b64 vcc, exec, s[44:45]
	v_pk_add_f32 v[26:27], v[20:21], v[40:41]
	v_pk_add_f32 v[20:21], v[18:19], v[38:39]
	v_cvt_pk_bf16_f32 v18, v22, v23
	v_cvt_pk_bf16_f32 v19, v24, v25
	s_waitcnt vmcnt(1) lgkmcnt(0)
	v_lshlrev_b32_e32 v28, 16, v37
	v_cvt_pk_bf16_f32 v20, v20, v21
	v_cvt_pk_bf16_f32 v21, v26, v27
	global_store_dwordx4 v[50:51], v[18:21], off offset:256
	v_lshlrev_b32_e32 v26, 16, v36
	v_and_b32_e32 v27, 0xffff0000, v36
	v_and_b32_e32 v29, 0xffff0000, v37
	v_lshlrev_b32_e32 v30, 16, v34
	v_and_b32_e32 v31, 0xffff0000, v34
	v_lshlrev_b32_e32 v32, 16, v35
	v_and_b32_e32 v33, 0xffff0000, v35
	v_lshlrev_b32_e32 v22, 16, v64
	v_and_b32_e32 v23, 0xffff0000, v64
	v_lshlrev_b32_e32 v24, 16, v65
	v_and_b32_e32 v25, 0xffff0000, v65
	v_pk_add_f32 v[16:17], v[16:17], v[32:33]
	v_pk_add_f32 v[14:15], v[14:15], v[30:31]
	v_pk_add_f32 v[28:29], v[12:13], v[28:29]
	v_pk_add_f32 v[12:13], v[10:11], v[26:27]
	v_cvt_pk_bf16_f32 v10, v14, v15
	v_cvt_pk_bf16_f32 v11, v16, v17
	v_lshlrev_b32_e32 v18, 16, v62
	v_and_b32_e32 v19, 0xffff0000, v62
	v_lshlrev_b32_e32 v20, 16, v63
	v_and_b32_e32 v21, 0xffff0000, v63
	v_cvt_pk_bf16_f32 v12, v12, v13
	v_cvt_pk_bf16_f32 v13, v28, v29
	global_store_dwordx4 v[60:61], v[10:13], off
	v_pk_add_f32 v[8:9], v[8:9], v[20:21]
	v_pk_add_f32 v[6:7], v[6:7], v[18:19]
	v_pk_add_f32 v[10:11], v[4:5], v[24:25]
	v_pk_add_f32 v[4:5], v[2:3], v[22:23]
	v_cvt_pk_bf16_f32 v2, v6, v7
	v_cvt_pk_bf16_f32 v3, v8, v9
	s_nop 0
	v_cvt_pk_bf16_f32 v4, v4, v5
	v_cvt_pk_bf16_f32 v5, v10, v11
	global_store_dwordx4 v[46:47], v[2:5], off offset:256
	s_cbranch_vccnz .LBB0_1424
	s_andn2_b64 vcc, exec, s[28:29]
	s_cbranch_vccnz .LBB0_1423
	s_barrier
	s_branch .LBB0_1423
